# post-barrier SALU / DMA-address ops of the K-loop segments hoisted in front of their s_barrier (16 sites, exact reorder across the barrier only)
# baseline (speedup 1.0000x reference)
.LBB0_285:
	ds_read_b128 v[18:21], v201
	ds_read_b128 v[22:25], v201 offset:1024
	ds_read_b128 v[26:29], v201 offset:2048
	ds_read_b128 v[30:33], v201 offset:3072
	ds_read_b128 v[2:5], v202
	ds_read_b128 v[6:9], v202 offset:1024
	ds_read_b128 v[10:13], v202 offset:2048
	ds_read_b128 v[14:17], v202 offset:3072
	s_add_u32 s62, s58, 0xfffc0080
	s_addc_u32 s63, s59, -1
	s_cmp_eq_u32 s71, 12
	s_cselect_b32 s67, s43, s63
	s_cselect_b32 s66, s57, s62
	s_cselect_b32 s63, s45, s70
	s_cselect_b32 s62, s68, s69
	v_lshl_add_u64 v[232:233], s[58:59], 0, v[172:173]
	s_add_i32 m0, s55, 0xc000
	ds_read_b128 v[176:179], v203
	ds_read_b128 v[180:183], v203 offset:1024
	ds_read_b128 v[206:209], v203 offset:2048
	ds_read_b128 v[210:213], v203 offset:3072
	ds_read_b128 v[214:217], v203 offset:4096
	ds_read_b128 v[218:221], v203 offset:5120
	ds_read_b128 v[222:225], v203 offset:6144
	ds_read_b128 v[226:229], v203 offset:7168
	global_load_lds_dwordx4 v[232:233], off
	v_lshl_add_u64 v[232:233], s[58:59], 0, v[174:175]
	s_add_i32 m0, s55, 0xe000
	s_nop 0
	global_load_lds_dwordx4 v[232:233], off
	s_waitcnt vmcnt(8)
	s_waitcnt lgkmcnt(0)
	s_barrier
	s_setprio 1
	s_waitcnt lgkmcnt(0)
	v_mfma_scale_f32_16x16x128_f8f6f4 v[158:161], v[18:25], v[176:183], v[158:161], v204, v204 op_sel_hi:[0,0,0]
	v_mfma_scale_f32_16x16x128_f8f6f4 v[154:157], v[26:33], v[176:183], v[154:157], v204, v204 op_sel_hi:[0,0,0]
	v_mfma_scale_f32_16x16x128_f8f6f4 v[150:153], v[18:25], v[206:213], v[150:153], v204, v204 op_sel_hi:[0,0,0]
	v_mfma_scale_f32_16x16x128_f8f6f4 v[146:149], v[26:33], v[206:213], v[146:149], v204, v204 op_sel_hi:[0,0,0]
	v_mfma_scale_f32_16x16x128_f8f6f4 v[130:133], v[18:25], v[214:221], v[130:133], v204, v204 op_sel_hi:[0,0,0]
	v_mfma_scale_f32_16x16x128_f8f6f4 v[122:125], v[26:33], v[214:221], v[122:125], v204, v204 op_sel_hi:[0,0,0]
	v_mfma_scale_f32_16x16x128_f8f6f4 v[118:121], v[18:25], v[222:229], v[118:121], v204, v204 op_sel_hi:[0,0,0]
	v_mfma_scale_f32_16x16x128_f8f6f4 v[114:117], v[26:33], v[222:229], v[114:117], v204, v204 op_sel_hi:[0,0,0]
	s_setprio 0
	s_setprio 1
	v_mfma_scale_f32_16x16x128_f8f6f4 v[142:145], v[2:9], v[176:183], v[142:145], v204, v204 op_sel_hi:[0,0,0]
	v_mfma_scale_f32_16x16x128_f8f6f4 v[138:141], v[10:17], v[176:183], v[138:141], v204, v204 op_sel_hi:[0,0,0]
	v_mfma_scale_f32_16x16x128_f8f6f4 v[134:137], v[2:9], v[206:213], v[134:137], v204, v204 op_sel_hi:[0,0,0]
	v_mfma_scale_f32_16x16x128_f8f6f4 v[126:129], v[10:17], v[206:213], v[126:129], v204, v204 op_sel_hi:[0,0,0]
	v_mfma_scale_f32_16x16x128_f8f6f4 v[110:113], v[2:9], v[214:221], v[110:113], v204, v204 op_sel_hi:[0,0,0]
	v_mfma_scale_f32_16x16x128_f8f6f4 v[106:109], v[10:17], v[214:221], v[106:109], v204, v204 op_sel_hi:[0,0,0]
	v_mfma_scale_f32_16x16x128_f8f6f4 v[102:105], v[2:9], v[222:229], v[102:105], v204, v204 op_sel_hi:[0,0,0]
	v_mfma_scale_f32_16x16x128_f8f6f4 v[98:101], v[10:17], v[222:229], v[98:101], v204, v204 op_sel_hi:[0,0,0]
	s_setprio 0
	s_add_i32 vcc_lo, s97, s39
	v_lshl_add_u64 v[176:177], s[62:63], 0, v[164:165]
	s_mov_b32 m0, vcc_lo
	s_barrier
	ds_read_b128 v[206:209], v203 offset:16384
	ds_read_b128 v[210:213], v203 offset:17408
	ds_read_b128 v[214:217], v203 offset:18432
	ds_read_b128 v[218:221], v203 offset:19456
	ds_read_b128 v[222:225], v203 offset:20480
	ds_read_b128 v[226:229], v203 offset:21504
	ds_read_b128 v[232:235], v203 offset:22528
	ds_read_b128 v[236:239], v203 offset:23552
	global_load_lds_dwordx4 v[176:177], off
	s_add_i32 m0, vcc_lo, 0x2000
	s_add_u32 vcc_lo, s62, 0x40000
	v_lshl_add_u64 v[178:179], s[62:63], 0, v[168:169]
	s_addc_u32 vcc_hi, s63, 0
	s_add_i32 s18, s34, s39
	global_load_lds_dwordx4 v[178:179], off
	v_lshl_add_u64 v[180:181], vcc, 0, v[164:165]
	s_mov_b32 m0, s18
	v_lshl_add_u64 v[182:183], s[66:67], 0, v[166:167]
	global_load_lds_dwordx4 v[180:181], off
	v_lshl_add_u64 v[180:181], vcc, 0, v[168:169]
	s_add_i32 m0, s18, 0x2000
	s_nop 0
	global_load_lds_dwordx4 v[180:181], off
	v_lshl_add_u64 v[180:181], s[66:67], 0, v[162:163]
	s_mov_b32 m0, s55
	s_nop 0
	global_load_lds_dwordx4 v[180:181], off
	s_mov_b32 m0, s90
	s_nop 0
	global_load_lds_dwordx4 v[182:183], off
	s_waitcnt vmcnt(8)
	s_waitcnt lgkmcnt(0)
	s_barrier
	s_setprio 1
	s_waitcnt lgkmcnt(0)
	v_mfma_scale_f32_16x16x128_f8f6f4 v[94:97], v[18:25], v[206:213], v[94:97], v204, v204 op_sel_hi:[0,0,0]
	v_mfma_scale_f32_16x16x128_f8f6f4 v[90:93], v[26:33], v[206:213], v[90:93], v204, v204 op_sel_hi:[0,0,0]
	v_mfma_scale_f32_16x16x128_f8f6f4 v[86:89], v[18:25], v[214:221], v[86:89], v204, v204 op_sel_hi:[0,0,0]
	v_mfma_scale_f32_16x16x128_f8f6f4 v[82:85], v[26:33], v[214:221], v[82:85], v204, v204 op_sel_hi:[0,0,0]
	v_mfma_scale_f32_16x16x128_f8f6f4 v[66:69], v[18:25], v[222:229], v[66:69], v204, v204 op_sel_hi:[0,0,0]
	v_mfma_scale_f32_16x16x128_f8f6f4 v[58:61], v[26:33], v[222:229], v[58:61], v204, v204 op_sel_hi:[0,0,0]
	v_mfma_scale_f32_16x16x128_f8f6f4 v[54:57], v[18:25], v[232:239], v[54:57], v204, v204 op_sel_hi:[0,0,0]
	v_mfma_scale_f32_16x16x128_f8f6f4 v[50:53], v[26:33], v[232:239], v[50:53], v204, v204 op_sel_hi:[0,0,0]
	s_setprio 0
	s_setprio 1
	v_mfma_scale_f32_16x16x128_f8f6f4 v[78:81], v[2:9], v[206:213], v[78:81], v204, v204 op_sel_hi:[0,0,0]
	v_mfma_scale_f32_16x16x128_f8f6f4 v[74:77], v[10:17], v[206:213], v[74:77], v204, v204 op_sel_hi:[0,0,0]
	v_mfma_scale_f32_16x16x128_f8f6f4 v[70:73], v[2:9], v[214:221], v[70:73], v204, v204 op_sel_hi:[0,0,0]
	v_mfma_scale_f32_16x16x128_f8f6f4 v[62:65], v[10:17], v[214:221], v[62:65], v204, v204 op_sel_hi:[0,0,0]
	v_mfma_scale_f32_16x16x128_f8f6f4 v[46:49], v[2:9], v[222:229], v[46:49], v204, v204 op_sel_hi:[0,0,0]
	v_mfma_scale_f32_16x16x128_f8f6f4 v[42:45], v[10:17], v[222:229], v[42:45], v204, v204 op_sel_hi:[0,0,0]
	v_mfma_scale_f32_16x16x128_f8f6f4 v[38:41], v[2:9], v[232:239], v[38:41], v204, v204 op_sel_hi:[0,0,0]
	v_mfma_scale_f32_16x16x128_f8f6f4 v[34:37], v[10:17], v[232:239], v[34:37], v204, v204 op_sel_hi:[0,0,0]
	s_setprio 0
	s_add_i32 s18, 0, 0x18000
	s_add_i32 s19, 0, 0x1c000
	s_barrier
	v_add_u32_e32 v14, s18, v198
	v_add_u32_e32 v30, s19, v198
	ds_read_b128 v[2:5], v14
	ds_read_b128 v[6:9], v14 offset:1024
	ds_read_b128 v[10:13], v14 offset:2048
	ds_read_b128 v[14:17], v14 offset:3072
	ds_read_b128 v[18:21], v30
	ds_read_b128 v[22:25], v30 offset:1024
	ds_read_b128 v[26:29], v30 offset:2048
	ds_read_b128 v[30:33], v30 offset:3072
	s_add_u32 s66, s66, 0x40000
	s_addc_u32 s67, s67, 0
	s_mov_b32 m0, s91
	v_lshl_add_u64 v[240:241], s[66:67], 0, v[162:163]
	ds_read_b128 v[206:209], v203 offset:32768
	ds_read_b128 v[210:213], v203 offset:33792
	ds_read_b128 v[214:217], v203 offset:34816
	ds_read_b128 v[218:221], v203 offset:35840
	ds_read_b128 v[222:225], v203 offset:36864
	ds_read_b128 v[226:229], v203 offset:37888
	ds_read_b128 v[232:235], v203 offset:38912
	ds_read_b128 v[236:239], v203 offset:39936
	global_load_lds_dwordx4 v[240:241], off
	v_lshl_add_u64 v[240:241], s[66:67], 0, v[166:167]
	s_mov_b32 m0, s92
	s_nop 0
	global_load_lds_dwordx4 v[240:241], off
	s_waitcnt vmcnt(8)
	s_waitcnt lgkmcnt(0)
	s_barrier
	s_setprio 1
	s_waitcnt lgkmcnt(0)
	v_mfma_scale_f32_16x16x128_f8f6f4 v[158:161], v[2:9], v[206:213], v[158:161], v204, v204 op_sel_hi:[0,0,0]
	v_mfma_scale_f32_16x16x128_f8f6f4 v[154:157], v[10:17], v[206:213], v[154:157], v204, v204 op_sel_hi:[0,0,0]
	v_mfma_scale_f32_16x16x128_f8f6f4 v[150:153], v[2:9], v[214:221], v[150:153], v204, v204 op_sel_hi:[0,0,0]
	v_mfma_scale_f32_16x16x128_f8f6f4 v[146:149], v[10:17], v[214:221], v[146:149], v204, v204 op_sel_hi:[0,0,0]
	v_mfma_scale_f32_16x16x128_f8f6f4 v[130:133], v[2:9], v[222:229], v[130:133], v204, v204 op_sel_hi:[0,0,0]
	v_mfma_scale_f32_16x16x128_f8f6f4 v[122:125], v[10:17], v[222:229], v[122:125], v204, v204 op_sel_hi:[0,0,0]
	v_mfma_scale_f32_16x16x128_f8f6f4 v[118:121], v[2:9], v[232:239], v[118:121], v204, v204 op_sel_hi:[0,0,0]
	v_mfma_scale_f32_16x16x128_f8f6f4 v[114:117], v[10:17], v[232:239], v[114:117], v204, v204 op_sel_hi:[0,0,0]
	s_setprio 0
	s_setprio 1
	v_mfma_scale_f32_16x16x128_f8f6f4 v[142:145], v[18:25], v[206:213], v[142:145], v204, v204 op_sel_hi:[0,0,0]
	v_mfma_scale_f32_16x16x128_f8f6f4 v[138:141], v[26:33], v[206:213], v[138:141], v204, v204 op_sel_hi:[0,0,0]
	v_mfma_scale_f32_16x16x128_f8f6f4 v[134:137], v[18:25], v[214:221], v[134:137], v204, v204 op_sel_hi:[0,0,0]
	v_mfma_scale_f32_16x16x128_f8f6f4 v[126:129], v[26:33], v[214:221], v[126:129], v204, v204 op_sel_hi:[0,0,0]
	v_mfma_scale_f32_16x16x128_f8f6f4 v[110:113], v[18:25], v[222:229], v[110:113], v204, v204 op_sel_hi:[0,0,0]
	v_mfma_scale_f32_16x16x128_f8f6f4 v[106:109], v[26:33], v[222:229], v[106:109], v204, v204 op_sel_hi:[0,0,0]
	v_mfma_scale_f32_16x16x128_f8f6f4 v[102:105], v[18:25], v[232:239], v[102:105], v204, v204 op_sel_hi:[0,0,0]
	v_mfma_scale_f32_16x16x128_f8f6f4 v[98:101], v[26:33], v[232:239], v[98:101], v204, v204 op_sel_hi:[0,0,0]
	s_setprio 0
	s_add_i32 s18, s18, s39
	v_lshl_add_u64 v[176:177], v[176:177], 0, s[14:15]
	s_mov_b32 m0, s18
	s_barrier
	ds_read_b128 v[206:209], v203 offset:49152
	ds_read_b128 v[210:213], v203 offset:50176
	ds_read_b128 v[214:217], v203 offset:51200
	ds_read_b128 v[218:221], v203 offset:52224
	ds_read_b128 v[222:225], v203 offset:53248
	ds_read_b128 v[226:229], v203 offset:54272
	ds_read_b128 v[232:235], v203 offset:55296
	ds_read_b128 v[236:239], v203 offset:56320
	global_load_lds_dwordx4 v[176:177], off
	s_add_i32 m0, s18, 0x2000
	s_add_u32 s62, s62, 0x40080
	v_lshl_add_u64 v[176:177], v[178:179], 0, s[14:15]
	s_addc_u32 s63, s63, 0
	s_add_i32 s18, s19, s39
	global_load_lds_dwordx4 v[176:177], off
	v_lshl_add_u64 v[176:177], s[62:63], 0, v[164:165]
	s_mov_b32 m0, s18
	s_nop 0
	global_load_lds_dwordx4 v[176:177], off
	v_lshl_add_u64 v[176:177], s[62:63], 0, v[168:169]
	s_add_i32 m0, s18, 0x2000
	s_nop 0
	global_load_lds_dwordx4 v[176:177], off
	v_lshl_add_u64 v[176:177], v[180:181], 0, s[14:15]
	s_mov_b32 m0, s93
	s_nop 0
	global_load_lds_dwordx4 v[176:177], off
	v_lshl_add_u64 v[176:177], v[182:183], 0, s[14:15]
	s_mov_b32 m0, s95
	s_nop 0
	global_load_lds_dwordx4 v[176:177], off
	s_waitcnt vmcnt(8)
	s_waitcnt lgkmcnt(0)
	s_barrier
	s_setprio 1
	s_waitcnt lgkmcnt(0)
	v_mfma_scale_f32_16x16x128_f8f6f4 v[94:97], v[2:9], v[206:213], v[94:97], v204, v204 op_sel_hi:[0,0,0]
	v_mfma_scale_f32_16x16x128_f8f6f4 v[90:93], v[10:17], v[206:213], v[90:93], v204, v204 op_sel_hi:[0,0,0]
	v_mfma_scale_f32_16x16x128_f8f6f4 v[86:89], v[2:9], v[214:221], v[86:89], v204, v204 op_sel_hi:[0,0,0]
	v_mfma_scale_f32_16x16x128_f8f6f4 v[82:85], v[10:17], v[214:221], v[82:85], v204, v204 op_sel_hi:[0,0,0]
	v_mfma_scale_f32_16x16x128_f8f6f4 v[66:69], v[2:9], v[222:229], v[66:69], v204, v204 op_sel_hi:[0,0,0]
	v_mfma_scale_f32_16x16x128_f8f6f4 v[58:61], v[10:17], v[222:229], v[58:61], v204, v204 op_sel_hi:[0,0,0]
	v_mfma_scale_f32_16x16x128_f8f6f4 v[54:57], v[2:9], v[232:239], v[54:57], v204, v204 op_sel_hi:[0,0,0]
	v_mfma_scale_f32_16x16x128_f8f6f4 v[50:53], v[10:17], v[232:239], v[50:53], v204, v204 op_sel_hi:[0,0,0]
	s_setprio 0
	s_setprio 1
	v_mfma_scale_f32_16x16x128_f8f6f4 v[78:81], v[18:25], v[206:213], v[78:81], v204, v204 op_sel_hi:[0,0,0]
	v_mfma_scale_f32_16x16x128_f8f6f4 v[74:77], v[26:33], v[206:213], v[74:77], v204, v204 op_sel_hi:[0,0,0]
	v_mfma_scale_f32_16x16x128_f8f6f4 v[70:73], v[18:25], v[214:221], v[70:73], v204, v204 op_sel_hi:[0,0,0]
	v_mfma_scale_f32_16x16x128_f8f6f4 v[62:65], v[26:33], v[214:221], v[62:65], v204, v204 op_sel_hi:[0,0,0]
	v_mfma_scale_f32_16x16x128_f8f6f4 v[46:49], v[18:25], v[222:229], v[46:49], v204, v204 op_sel_hi:[0,0,0]
	v_mfma_scale_f32_16x16x128_f8f6f4 v[42:45], v[26:33], v[222:229], v[42:45], v204, v204 op_sel_hi:[0,0,0]
	v_mfma_scale_f32_16x16x128_f8f6f4 v[38:41], v[18:25], v[232:239], v[38:41], v204, v204 op_sel_hi:[0,0,0]
	v_mfma_scale_f32_16x16x128_f8f6f4 v[34:37], v[26:33], v[232:239], v[34:37], v204, v204 op_sel_hi:[0,0,0]
	s_setprio 0
	s_add_i32 s71, s71, 2
	s_add_u32 s58, s58, 0x100
	s_addc_u32 s59, s59, 0
	s_add_u32 s69, s69, 0x100
	s_addc_u32 s70, s70, 0
	s_cmp_gt_u32 s71, 13
	s_barrier
	s_cbranch_scc0 .LBB0_285
	s_and_b64 vcc, exec, s[16:17]
	s_cbranch_vccz .LBB0_288
	s_barrier

.LBB0_336:
	ds_read_b128 v[142:145], v1
	ds_read_b128 v[152:155], v1 offset:1024
	ds_read_b128 v[156:159], v1 offset:2048
	ds_read_b128 v[160:163], v1 offset:3072
	ds_read_b128 v[164:167], v149
	ds_read_b128 v[168:171], v149 offset:1024
	ds_read_b128 v[172:175], v149 offset:2048
	ds_read_b128 v[176:179], v149 offset:3072
	s_add_u32 s18, s48, 0xfff80080
	s_addc_u32 s19, s49, -1
	s_cmp_eq_u32 s87, 28
	s_cselect_b32 s55, s17, s19
	s_cselect_b32 s54, s56, s18
	s_cselect_b32 s53, s39, s59
	s_cselect_b32 s52, s57, s58
	v_lshl_add_u64 v[212:213], s[48:49], 0, v[138:139]
	s_add_i32 m0, s47, 0xc000
	ds_read_b128 v[180:183], v150
	ds_read_b128 v[184:187], v150 offset:1024
	ds_read_b128 v[188:191], v150 offset:2048
	ds_read_b128 v[192:195], v150 offset:3072
	ds_read_b128 v[196:199], v150 offset:4096
	ds_read_b128 v[200:203], v150 offset:5120
	ds_read_b128 v[204:207], v150 offset:6144
	ds_read_b128 v[208:211], v150 offset:7168
	global_load_lds_dwordx4 v[212:213], off
	v_lshl_add_u64 v[212:213], s[48:49], 0, v[140:141]
	s_add_i32 m0, s47, 0xe000
	s_nop 0
	global_load_lds_dwordx4 v[212:213], off
	s_waitcnt vmcnt(8)
	s_waitcnt lgkmcnt(0)
	s_barrier
	s_setprio 1
	s_waitcnt lgkmcnt(0)
	v_mfma_f32_16x16x32_bf16 v[126:129], v[142:145], v[180:183], v[126:129]
	v_mfma_f32_16x16x32_bf16 v[122:125], v[156:159], v[180:183], v[122:125]
	v_mfma_f32_16x16x32_bf16 v[114:117], v[142:145], v[188:191], v[114:117]
	v_mfma_f32_16x16x32_bf16 v[106:109], v[156:159], v[188:191], v[106:109]
	v_mfma_f32_16x16x32_bf16 v[98:101], v[142:145], v[196:199], v[98:101]
	v_mfma_f32_16x16x32_bf16 v[90:93], v[156:159], v[196:199], v[90:93]
	v_mfma_f32_16x16x32_bf16 v[82:85], v[142:145], v[204:207], v[82:85]
	v_mfma_f32_16x16x32_bf16 v[74:77], v[156:159], v[204:207], v[74:77]
	v_mfma_f32_16x16x32_bf16 v[126:129], v[152:155], v[184:187], v[126:129]
	v_mfma_f32_16x16x32_bf16 v[122:125], v[160:163], v[184:187], v[122:125]
	v_mfma_f32_16x16x32_bf16 v[114:117], v[152:155], v[192:195], v[114:117]
	v_mfma_f32_16x16x32_bf16 v[106:109], v[160:163], v[192:195], v[106:109]
	v_mfma_f32_16x16x32_bf16 v[98:101], v[152:155], v[200:203], v[98:101]
	v_mfma_f32_16x16x32_bf16 v[90:93], v[160:163], v[200:203], v[90:93]
	v_mfma_f32_16x16x32_bf16 v[82:85], v[152:155], v[208:211], v[82:85]
	v_mfma_f32_16x16x32_bf16 v[74:77], v[160:163], v[208:211], v[74:77]
	s_setprio 0
	s_setprio 1
	v_mfma_f32_16x16x32_bf16 v[118:121], v[164:167], v[180:183], v[118:121]
	v_mfma_f32_16x16x32_bf16 v[110:113], v[172:175], v[180:183], v[110:113]
	v_mfma_f32_16x16x32_bf16 v[102:105], v[164:167], v[188:191], v[102:105]
	v_mfma_f32_16x16x32_bf16 v[94:97], v[172:175], v[188:191], v[94:97]
	v_mfma_f32_16x16x32_bf16 v[86:89], v[164:167], v[196:199], v[86:89]
	v_mfma_f32_16x16x32_bf16 v[78:81], v[172:175], v[196:199], v[78:81]
	v_mfma_f32_16x16x32_bf16 v[70:73], v[164:167], v[204:207], v[70:73]
	v_mfma_f32_16x16x32_bf16 v[66:69], v[172:175], v[204:207], v[66:69]
	v_mfma_f32_16x16x32_bf16 v[118:121], v[168:171], v[184:187], v[118:121]
	v_mfma_f32_16x16x32_bf16 v[110:113], v[176:179], v[184:187], v[110:113]
	v_mfma_f32_16x16x32_bf16 v[102:105], v[168:171], v[192:195], v[102:105]
	v_mfma_f32_16x16x32_bf16 v[94:97], v[176:179], v[192:195], v[94:97]
	v_mfma_f32_16x16x32_bf16 v[86:89], v[168:171], v[200:203], v[86:89]
	v_mfma_f32_16x16x32_bf16 v[78:81], v[176:179], v[200:203], v[78:81]
	v_mfma_f32_16x16x32_bf16 v[70:73], v[168:171], v[208:211], v[70:73]
	v_mfma_f32_16x16x32_bf16 v[66:69], v[176:179], v[208:211], v[66:69]
	s_setprio 0
	s_add_i32 s18, s71, s30
	v_lshl_add_u64 v[212:213], s[52:53], 0, v[132:133]
	s_mov_b32 m0, s18
	s_barrier
	ds_read_b128 v[180:183], v150 offset:16384
	ds_read_b128 v[184:187], v150 offset:17408
	ds_read_b128 v[188:191], v150 offset:18432
	ds_read_b128 v[192:195], v150 offset:19456
	ds_read_b128 v[196:199], v150 offset:20480
	ds_read_b128 v[200:203], v150 offset:21504
	ds_read_b128 v[204:207], v150 offset:22528
	ds_read_b128 v[208:211], v150 offset:23552
	global_load_lds_dwordx4 v[212:213], off
	s_add_i32 m0, s18, 0x2000
	s_add_u32 s90, s52, 0x80000
	v_lshl_add_u64 v[214:215], s[52:53], 0, v[136:137]
	s_addc_u32 s91, s53, 0
	s_add_i32 s18, s84, s30
	global_load_lds_dwordx4 v[214:215], off
	v_lshl_add_u64 v[216:217], s[90:91], 0, v[132:133]
	s_mov_b32 m0, s18
	v_lshl_add_u64 v[218:219], s[54:55], 0, v[134:135]
	global_load_lds_dwordx4 v[216:217], off
	v_lshl_add_u64 v[216:217], s[90:91], 0, v[136:137]
	s_add_i32 m0, s18, 0x2000
	s_nop 0
	global_load_lds_dwordx4 v[216:217], off
	v_lshl_add_u64 v[216:217], s[54:55], 0, v[130:131]
	s_mov_b32 m0, s47
	s_nop 0
	global_load_lds_dwordx4 v[216:217], off
	s_mov_b32 m0, s63
	s_nop 0
	global_load_lds_dwordx4 v[218:219], off
	s_waitcnt vmcnt(8)
	s_waitcnt lgkmcnt(0)
	s_barrier
	s_setprio 1
	s_waitcnt lgkmcnt(0)
	v_mfma_f32_16x16x32_bf16 v[62:65], v[142:145], v[180:183], v[62:65]
	v_mfma_f32_16x16x32_bf16 v[58:61], v[156:159], v[180:183], v[58:61]
	v_mfma_f32_16x16x32_bf16 v[50:53], v[142:145], v[188:191], v[50:53]
	v_mfma_f32_16x16x32_bf16 v[42:45], v[156:159], v[188:191], v[42:45]
	v_mfma_f32_16x16x32_bf16 v[34:37], v[142:145], v[196:199], v[34:37]
	v_mfma_f32_16x16x32_bf16 v[26:29], v[156:159], v[196:199], v[26:29]
	v_mfma_f32_16x16x32_bf16 v[18:21], v[142:145], v[204:207], v[18:21]
	v_mfma_f32_16x16x32_bf16 v[10:13], v[156:159], v[204:207], v[10:13]
	v_mfma_f32_16x16x32_bf16 v[62:65], v[152:155], v[184:187], v[62:65]
	v_mfma_f32_16x16x32_bf16 v[58:61], v[160:163], v[184:187], v[58:61]
	v_mfma_f32_16x16x32_bf16 v[50:53], v[152:155], v[192:195], v[50:53]
	v_mfma_f32_16x16x32_bf16 v[42:45], v[160:163], v[192:195], v[42:45]
	v_mfma_f32_16x16x32_bf16 v[34:37], v[152:155], v[200:203], v[34:37]
	v_mfma_f32_16x16x32_bf16 v[26:29], v[160:163], v[200:203], v[26:29]
	v_mfma_f32_16x16x32_bf16 v[18:21], v[152:155], v[208:211], v[18:21]
	v_mfma_f32_16x16x32_bf16 v[10:13], v[160:163], v[208:211], v[10:13]
	s_setprio 0
	s_setprio 1
	v_mfma_f32_16x16x32_bf16 v[54:57], v[164:167], v[180:183], v[54:57]
	v_mfma_f32_16x16x32_bf16 v[46:49], v[172:175], v[180:183], v[46:49]
	v_mfma_f32_16x16x32_bf16 v[38:41], v[164:167], v[188:191], v[38:41]
	v_mfma_f32_16x16x32_bf16 v[30:33], v[172:175], v[188:191], v[30:33]
	v_mfma_f32_16x16x32_bf16 v[22:25], v[164:167], v[196:199], v[22:25]
	v_mfma_f32_16x16x32_bf16 v[14:17], v[172:175], v[196:199], v[14:17]
	v_mfma_f32_16x16x32_bf16 v[6:9], v[164:167], v[204:207], v[6:9]
	v_mfma_f32_16x16x32_bf16 v[2:5], v[172:175], v[204:207], v[2:5]
	v_mfma_f32_16x16x32_bf16 v[54:57], v[168:171], v[184:187], v[54:57]
	v_mfma_f32_16x16x32_bf16 v[46:49], v[176:179], v[184:187], v[46:49]
	v_mfma_f32_16x16x32_bf16 v[38:41], v[168:171], v[192:195], v[38:41]
	v_mfma_f32_16x16x32_bf16 v[30:33], v[176:179], v[192:195], v[30:33]
	v_mfma_f32_16x16x32_bf16 v[22:25], v[168:171], v[200:203], v[22:25]
	v_mfma_f32_16x16x32_bf16 v[14:17], v[176:179], v[200:203], v[14:17]
	v_mfma_f32_16x16x32_bf16 v[6:9], v[168:171], v[208:211], v[6:9]
	v_mfma_f32_16x16x32_bf16 v[2:5], v[176:179], v[208:211], v[2:5]
	s_setprio 0
	s_add_i32 s18, 0, 0x18000
	s_barrier
	v_add_u32_e32 v151, s18, v147
	s_add_i32 s19, 0, 0x1c000
	ds_read_b128 v[142:145], v151
	ds_read_b128 v[152:155], v151 offset:1024
	ds_read_b128 v[156:159], v151 offset:2048
	ds_read_b128 v[160:163], v151 offset:3072
	v_add_u32_e32 v151, s19, v147
	ds_read_b128 v[164:167], v151
	ds_read_b128 v[168:171], v151 offset:1024
	ds_read_b128 v[172:175], v151 offset:2048
	ds_read_b128 v[176:179], v151 offset:3072
	s_add_u32 s54, s54, 0x80000
	s_addc_u32 s55, s55, 0
	s_mov_b32 m0, s66
	v_lshl_add_u64 v[220:221], s[54:55], 0, v[130:131]
	ds_read_b128 v[180:183], v150 offset:32768
	ds_read_b128 v[184:187], v150 offset:33792
	ds_read_b128 v[188:191], v150 offset:34816
	ds_read_b128 v[192:195], v150 offset:35840
	ds_read_b128 v[196:199], v150 offset:36864
	ds_read_b128 v[200:203], v150 offset:37888
	ds_read_b128 v[204:207], v150 offset:38912
	ds_read_b128 v[208:211], v150 offset:39936
	global_load_lds_dwordx4 v[220:221], off
	v_lshl_add_u64 v[220:221], s[54:55], 0, v[134:135]
	s_mov_b32 m0, s67
	s_nop 0
	global_load_lds_dwordx4 v[220:221], off
	s_waitcnt vmcnt(8)
	s_waitcnt lgkmcnt(0)
	s_barrier
	s_setprio 1
	s_waitcnt lgkmcnt(0)
	v_mfma_f32_16x16x32_bf16 v[126:129], v[142:145], v[180:183], v[126:129]
	v_mfma_f32_16x16x32_bf16 v[122:125], v[156:159], v[180:183], v[122:125]
	v_mfma_f32_16x16x32_bf16 v[114:117], v[142:145], v[188:191], v[114:117]
	v_mfma_f32_16x16x32_bf16 v[106:109], v[156:159], v[188:191], v[106:109]
	v_mfma_f32_16x16x32_bf16 v[98:101], v[142:145], v[196:199], v[98:101]
	v_mfma_f32_16x16x32_bf16 v[90:93], v[156:159], v[196:199], v[90:93]
	v_mfma_f32_16x16x32_bf16 v[82:85], v[142:145], v[204:207], v[82:85]
	v_mfma_f32_16x16x32_bf16 v[74:77], v[156:159], v[204:207], v[74:77]
	v_mfma_f32_16x16x32_bf16 v[126:129], v[152:155], v[184:187], v[126:129]
	v_mfma_f32_16x16x32_bf16 v[122:125], v[160:163], v[184:187], v[122:125]
	v_mfma_f32_16x16x32_bf16 v[114:117], v[152:155], v[192:195], v[114:117]
	v_mfma_f32_16x16x32_bf16 v[106:109], v[160:163], v[192:195], v[106:109]
	v_mfma_f32_16x16x32_bf16 v[98:101], v[152:155], v[200:203], v[98:101]
	v_mfma_f32_16x16x32_bf16 v[90:93], v[160:163], v[200:203], v[90:93]
	v_mfma_f32_16x16x32_bf16 v[82:85], v[152:155], v[208:211], v[82:85]
	v_mfma_f32_16x16x32_bf16 v[74:77], v[160:163], v[208:211], v[74:77]
	s_setprio 0
	s_setprio 1
	v_mfma_f32_16x16x32_bf16 v[118:121], v[164:167], v[180:183], v[118:121]
	v_mfma_f32_16x16x32_bf16 v[110:113], v[172:175], v[180:183], v[110:113]
	v_mfma_f32_16x16x32_bf16 v[102:105], v[164:167], v[188:191], v[102:105]
	v_mfma_f32_16x16x32_bf16 v[94:97], v[172:175], v[188:191], v[94:97]
	v_mfma_f32_16x16x32_bf16 v[86:89], v[164:167], v[196:199], v[86:89]
	v_mfma_f32_16x16x32_bf16 v[78:81], v[172:175], v[196:199], v[78:81]
	v_mfma_f32_16x16x32_bf16 v[70:73], v[164:167], v[204:207], v[70:73]
	v_mfma_f32_16x16x32_bf16 v[66:69], v[172:175], v[204:207], v[66:69]
	v_mfma_f32_16x16x32_bf16 v[118:121], v[168:171], v[184:187], v[118:121]
	v_mfma_f32_16x16x32_bf16 v[110:113], v[176:179], v[184:187], v[110:113]
	v_mfma_f32_16x16x32_bf16 v[102:105], v[168:171], v[192:195], v[102:105]
	v_mfma_f32_16x16x32_bf16 v[94:97], v[176:179], v[192:195], v[94:97]
	v_mfma_f32_16x16x32_bf16 v[86:89], v[168:171], v[200:203], v[86:89]
	v_mfma_f32_16x16x32_bf16 v[78:81], v[176:179], v[200:203], v[78:81]
	v_mfma_f32_16x16x32_bf16 v[70:73], v[168:171], v[208:211], v[70:73]
	v_mfma_f32_16x16x32_bf16 v[66:69], v[176:179], v[208:211], v[66:69]
	s_setprio 0
	s_add_i32 s18, s18, s30
	v_lshl_add_u64 v[212:213], v[212:213], 0, s[12:13]
	s_mov_b32 m0, s18
	s_barrier
	ds_read_b128 v[180:183], v150 offset:49152
	ds_read_b128 v[184:187], v150 offset:50176
	ds_read_b128 v[188:191], v150 offset:51200
	ds_read_b128 v[192:195], v150 offset:52224
	ds_read_b128 v[196:199], v150 offset:53248
	ds_read_b128 v[200:203], v150 offset:54272
	ds_read_b128 v[204:207], v150 offset:55296
	ds_read_b128 v[208:211], v150 offset:56320
	global_load_lds_dwordx4 v[212:213], off
	s_add_i32 m0, s18, 0x2000
	s_add_u32 s52, s52, 0x80080
	v_lshl_add_u64 v[212:213], v[214:215], 0, s[12:13]
	s_addc_u32 s53, s53, 0
	s_add_i32 s18, s19, s30
	global_load_lds_dwordx4 v[212:213], off
	v_lshl_add_u64 v[212:213], s[52:53], 0, v[132:133]
	s_mov_b32 m0, s18
	s_nop 0
	global_load_lds_dwordx4 v[212:213], off
	v_lshl_add_u64 v[212:213], s[52:53], 0, v[136:137]
	s_add_i32 m0, s18, 0x2000
	s_nop 0
	global_load_lds_dwordx4 v[212:213], off
	v_lshl_add_u64 v[212:213], v[216:217], 0, s[12:13]
	s_mov_b32 m0, s68
	s_nop 0
	global_load_lds_dwordx4 v[212:213], off
	v_lshl_add_u64 v[212:213], v[218:219], 0, s[12:13]
	s_mov_b32 m0, s69
	s_nop 0
	global_load_lds_dwordx4 v[212:213], off
	s_waitcnt vmcnt(8)
	s_waitcnt lgkmcnt(0)
	s_barrier
	s_setprio 1
	s_waitcnt lgkmcnt(0)
	v_mfma_f32_16x16x32_bf16 v[62:65], v[142:145], v[180:183], v[62:65]
	v_mfma_f32_16x16x32_bf16 v[58:61], v[156:159], v[180:183], v[58:61]
	v_mfma_f32_16x16x32_bf16 v[50:53], v[142:145], v[188:191], v[50:53]
	v_mfma_f32_16x16x32_bf16 v[42:45], v[156:159], v[188:191], v[42:45]
	v_mfma_f32_16x16x32_bf16 v[34:37], v[142:145], v[196:199], v[34:37]
	v_mfma_f32_16x16x32_bf16 v[26:29], v[156:159], v[196:199], v[26:29]
	v_mfma_f32_16x16x32_bf16 v[18:21], v[142:145], v[204:207], v[18:21]
	v_mfma_f32_16x16x32_bf16 v[10:13], v[156:159], v[204:207], v[10:13]
	v_mfma_f32_16x16x32_bf16 v[62:65], v[152:155], v[184:187], v[62:65]
	v_mfma_f32_16x16x32_bf16 v[58:61], v[160:163], v[184:187], v[58:61]
	v_mfma_f32_16x16x32_bf16 v[50:53], v[152:155], v[192:195], v[50:53]
	v_mfma_f32_16x16x32_bf16 v[42:45], v[160:163], v[192:195], v[42:45]
	v_mfma_f32_16x16x32_bf16 v[34:37], v[152:155], v[200:203], v[34:37]
	v_mfma_f32_16x16x32_bf16 v[26:29], v[160:163], v[200:203], v[26:29]
	v_mfma_f32_16x16x32_bf16 v[18:21], v[152:155], v[208:211], v[18:21]
	v_mfma_f32_16x16x32_bf16 v[10:13], v[160:163], v[208:211], v[10:13]
	s_setprio 0
	s_setprio 1
	v_mfma_f32_16x16x32_bf16 v[54:57], v[164:167], v[180:183], v[54:57]
	v_mfma_f32_16x16x32_bf16 v[46:49], v[172:175], v[180:183], v[46:49]
	v_mfma_f32_16x16x32_bf16 v[38:41], v[164:167], v[188:191], v[38:41]
	v_mfma_f32_16x16x32_bf16 v[30:33], v[172:175], v[188:191], v[30:33]
	v_mfma_f32_16x16x32_bf16 v[22:25], v[164:167], v[196:199], v[22:25]
	v_mfma_f32_16x16x32_bf16 v[14:17], v[172:175], v[196:199], v[14:17]
	v_mfma_f32_16x16x32_bf16 v[6:9], v[164:167], v[204:207], v[6:9]
	v_mfma_f32_16x16x32_bf16 v[2:5], v[172:175], v[204:207], v[2:5]
	v_mfma_f32_16x16x32_bf16 v[54:57], v[168:171], v[184:187], v[54:57]
	v_mfma_f32_16x16x32_bf16 v[46:49], v[176:179], v[184:187], v[46:49]
	v_mfma_f32_16x16x32_bf16 v[38:41], v[168:171], v[192:195], v[38:41]
	v_mfma_f32_16x16x32_bf16 v[30:33], v[176:179], v[192:195], v[30:33]
	v_mfma_f32_16x16x32_bf16 v[22:25], v[168:171], v[200:203], v[22:25]
	v_mfma_f32_16x16x32_bf16 v[14:17], v[176:179], v[200:203], v[14:17]
	v_mfma_f32_16x16x32_bf16 v[6:9], v[168:171], v[208:211], v[6:9]
	v_mfma_f32_16x16x32_bf16 v[2:5], v[176:179], v[208:211], v[2:5]
	s_setprio 0
	s_add_i32 s87, s87, 2
	s_add_u32 s48, s48, 0x100
	s_addc_u32 s49, s49, 0
	s_add_u32 s58, s58, 0x100
	s_addc_u32 s59, s59, 0
	s_cmp_gt_u32 s87, 29
	s_barrier
	s_cbranch_scc0 .LBB0_336
	s_and_b64 vcc, exec, s[14:15]
	s_cbranch_vccz .LBB0_339
	s_barrier

.LBB0_846:
	v_add_u32_e32 v2, s77, v162
	ds_read_b128 v[150:153], v2
	ds_read_b128 v[154:157], v2 offset:1024
	ds_read_b128 v[158:161], v2 offset:2048
	ds_read_b128 v[166:169], v2 offset:3072
	v_add_u32_e32 v2, s78, v162
	ds_read_b128 v[170:173], v2
	ds_read_b128 v[174:177], v2 offset:1024
	ds_read_b128 v[178:181], v2 offset:2048
	ds_read_b128 v[182:185], v2 offset:3072
	s_add_u32 s18, s54, 0xfff80080
	s_addc_u32 s19, s55, -1
	s_cmp_eq_u32 s87, 28
	s_cselect_b32 s63, s34, s19
	s_cselect_b32 s62, s35, s18
	s_cselect_b32 s59, s45, s86
	s_cselect_b32 s58, s47, s57
	v_lshl_add_u64 v[4:5], s[54:55], 0, v[142:143]
	s_add_i32 m0, s71, 0xc000
	ds_read_b128 v[186:189], v164
	ds_read_b128 v[190:193], v164 offset:1024
	ds_read_b128 v[194:197], v164 offset:2048
	ds_read_b128 v[198:201], v164 offset:3072
	ds_read_b128 v[202:205], v164 offset:4096
	ds_read_b128 v[206:209], v164 offset:5120
	ds_read_b128 v[210:213], v164 offset:6144
	ds_read_b128 v[214:217], v164 offset:7168
	global_load_lds_dwordx4 v[4:5], off
	v_lshl_add_u64 v[4:5], s[54:55], 0, v[144:145]
	s_add_i32 m0, s71, 0xe000
	s_nop 0
	global_load_lds_dwordx4 v[4:5], off
	s_waitcnt vmcnt(8)
	s_waitcnt lgkmcnt(0)
	s_barrier
	s_setprio 1
	s_waitcnt lgkmcnt(0)
	v_mfma_f32_16x16x32_bf16 v[130:133], v[150:153], v[186:189], v[130:133]
	v_mfma_f32_16x16x32_bf16 v[126:129], v[158:161], v[186:189], v[126:129]
	v_mfma_f32_16x16x32_bf16 v[122:125], v[150:153], v[194:197], v[122:125]
	v_mfma_f32_16x16x32_bf16 v[118:121], v[158:161], v[194:197], v[118:121]
	v_mfma_f32_16x16x32_bf16 v[114:117], v[150:153], v[202:205], v[114:117]
	v_mfma_f32_16x16x32_bf16 v[110:113], v[158:161], v[202:205], v[110:113]
	v_mfma_f32_16x16x32_bf16 v[106:109], v[150:153], v[210:213], v[106:109]
	v_mfma_f32_16x16x32_bf16 v[102:105], v[158:161], v[210:213], v[102:105]
	v_mfma_f32_16x16x32_bf16 v[130:133], v[154:157], v[190:193], v[130:133]
	v_mfma_f32_16x16x32_bf16 v[126:129], v[166:169], v[190:193], v[126:129]
	v_mfma_f32_16x16x32_bf16 v[122:125], v[154:157], v[198:201], v[122:125]
	v_mfma_f32_16x16x32_bf16 v[118:121], v[166:169], v[198:201], v[118:121]
	v_mfma_f32_16x16x32_bf16 v[114:117], v[154:157], v[206:209], v[114:117]
	v_mfma_f32_16x16x32_bf16 v[110:113], v[166:169], v[206:209], v[110:113]
	v_mfma_f32_16x16x32_bf16 v[106:109], v[154:157], v[214:217], v[106:109]
	v_mfma_f32_16x16x32_bf16 v[102:105], v[166:169], v[214:217], v[102:105]
	s_setprio 0
	s_setprio 1
	v_mfma_f32_16x16x32_bf16 v[98:101], v[170:173], v[186:189], v[98:101]
	v_mfma_f32_16x16x32_bf16 v[94:97], v[178:181], v[186:189], v[94:97]
	v_mfma_f32_16x16x32_bf16 v[90:93], v[170:173], v[194:197], v[90:93]
	v_mfma_f32_16x16x32_bf16 v[86:89], v[178:181], v[194:197], v[86:89]
	v_mfma_f32_16x16x32_bf16 v[82:85], v[170:173], v[202:205], v[82:85]
	v_mfma_f32_16x16x32_bf16 v[78:81], v[178:181], v[202:205], v[78:81]
	v_mfma_f32_16x16x32_bf16 v[74:77], v[170:173], v[210:213], v[74:77]
	v_mfma_f32_16x16x32_bf16 v[70:73], v[178:181], v[210:213], v[70:73]
	v_mfma_f32_16x16x32_bf16 v[98:101], v[174:177], v[190:193], v[98:101]
	v_mfma_f32_16x16x32_bf16 v[94:97], v[182:185], v[190:193], v[94:97]
	v_mfma_f32_16x16x32_bf16 v[90:93], v[174:177], v[198:201], v[90:93]
	v_mfma_f32_16x16x32_bf16 v[86:89], v[182:185], v[198:201], v[86:89]
	v_mfma_f32_16x16x32_bf16 v[82:85], v[174:177], v[206:209], v[82:85]
	v_mfma_f32_16x16x32_bf16 v[78:81], v[182:185], v[206:209], v[78:81]
	v_mfma_f32_16x16x32_bf16 v[74:77], v[174:177], v[214:217], v[74:77]
	v_mfma_f32_16x16x32_bf16 v[70:73], v[182:185], v[214:217], v[70:73]
	s_setprio 0
	s_add_i32 s18, s77, s70
	v_lshl_add_u64 v[218:219], s[58:59], 0, v[136:137]
	s_mov_b32 m0, s18
	s_barrier
	ds_read_b128 v[186:189], v164 offset:16384
	ds_read_b128 v[190:193], v164 offset:17408
	ds_read_b128 v[194:197], v164 offset:18432
	ds_read_b128 v[198:201], v164 offset:19456
	ds_read_b128 v[202:205], v164 offset:20480
	ds_read_b128 v[206:209], v164 offset:21504
	ds_read_b128 v[210:213], v164 offset:22528
	ds_read_b128 v[214:217], v164 offset:23552
	global_load_lds_dwordx4 v[218:219], off
	s_add_i32 m0, s18, 0x2000
	s_add_u32 s90, s58, 0x80000
	v_lshl_add_u64 v[220:221], s[58:59], 0, v[140:141]
	s_addc_u32 s91, s59, 0
	s_add_i32 s18, s78, s70
	global_load_lds_dwordx4 v[220:221], off
	v_lshl_add_u64 v[4:5], s[90:91], 0, v[136:137]
	s_mov_b32 m0, s18
	v_lshl_add_u64 v[222:223], s[62:63], 0, v[134:135]
	global_load_lds_dwordx4 v[4:5], off
	v_lshl_add_u64 v[4:5], s[90:91], 0, v[140:141]
	s_add_i32 m0, s18, 0x2000
	v_lshl_add_u64 v[224:225], s[62:63], 0, v[138:139]
	global_load_lds_dwordx4 v[4:5], off
	s_mov_b32 m0, s71
	s_nop 0
	global_load_lds_dwordx4 v[222:223], off
	s_mov_b32 m0, s72
	s_nop 0
	global_load_lds_dwordx4 v[224:225], off
	s_waitcnt vmcnt(8)
	s_waitcnt lgkmcnt(0)
	s_barrier
	s_setprio 1
	s_waitcnt lgkmcnt(0)
	v_mfma_f32_16x16x32_bf16 v[66:69], v[150:153], v[186:189], v[66:69]
	v_mfma_f32_16x16x32_bf16 v[62:65], v[158:161], v[186:189], v[62:65]
	v_mfma_f32_16x16x32_bf16 v[58:61], v[150:153], v[194:197], v[58:61]
	v_mfma_f32_16x16x32_bf16 v[54:57], v[158:161], v[194:197], v[54:57]
	v_mfma_f32_16x16x32_bf16 v[50:53], v[150:153], v[202:205], v[50:53]
	v_mfma_f32_16x16x32_bf16 v[46:49], v[158:161], v[202:205], v[46:49]
	v_mfma_f32_16x16x32_bf16 v[42:45], v[150:153], v[210:213], v[42:45]
	v_mfma_f32_16x16x32_bf16 v[38:41], v[158:161], v[210:213], v[38:41]
	v_mfma_f32_16x16x32_bf16 v[66:69], v[154:157], v[190:193], v[66:69]
	v_mfma_f32_16x16x32_bf16 v[62:65], v[166:169], v[190:193], v[62:65]
	v_mfma_f32_16x16x32_bf16 v[58:61], v[154:157], v[198:201], v[58:61]
	v_mfma_f32_16x16x32_bf16 v[54:57], v[166:169], v[198:201], v[54:57]
	v_mfma_f32_16x16x32_bf16 v[50:53], v[154:157], v[206:209], v[50:53]
	v_mfma_f32_16x16x32_bf16 v[46:49], v[166:169], v[206:209], v[46:49]
	v_mfma_f32_16x16x32_bf16 v[42:45], v[154:157], v[214:217], v[42:45]
	v_mfma_f32_16x16x32_bf16 v[38:41], v[166:169], v[214:217], v[38:41]
	s_setprio 0
	s_setprio 1
	v_mfma_f32_16x16x32_bf16 v[34:37], v[170:173], v[186:189], v[34:37]
	v_mfma_f32_16x16x32_bf16 v[30:33], v[178:181], v[186:189], v[30:33]
	v_mfma_f32_16x16x32_bf16 v[26:29], v[170:173], v[194:197], v[26:29]
	v_mfma_f32_16x16x32_bf16 v[22:25], v[178:181], v[194:197], v[22:25]
	v_mfma_f32_16x16x32_bf16 v[18:21], v[170:173], v[202:205], v[18:21]
	v_mfma_f32_16x16x32_bf16 v[14:17], v[178:181], v[202:205], v[14:17]
	v_mfma_f32_16x16x32_bf16 v[10:13], v[170:173], v[210:213], v[10:13]
	v_mfma_f32_16x16x32_bf16 v[4:7], v[178:181], v[210:213], v[6:9]
	v_mfma_f32_16x16x32_bf16 v[34:37], v[174:177], v[190:193], v[34:37]
	v_mfma_f32_16x16x32_bf16 v[30:33], v[182:185], v[190:193], v[30:33]
	v_mfma_f32_16x16x32_bf16 v[26:29], v[174:177], v[198:201], v[26:29]
	v_mfma_f32_16x16x32_bf16 v[22:25], v[182:185], v[198:201], v[22:25]
	v_mfma_f32_16x16x32_bf16 v[18:21], v[174:177], v[206:209], v[18:21]
	v_mfma_f32_16x16x32_bf16 v[14:17], v[182:185], v[206:209], v[14:17]
	v_mfma_f32_16x16x32_bf16 v[10:13], v[174:177], v[214:217], v[10:13]
	v_mfma_f32_16x16x32_bf16 v[4:7], v[182:185], v[214:217], v[4:7]
	s_setprio 0
	s_add_i32 s18, 0, 0x18000
	s_barrier
	v_add_u32_e32 v2, s18, v162
	s_add_i32 s19, 0, 0x1c000
	ds_read_b128 v[150:153], v2
	ds_read_b128 v[154:157], v2 offset:1024
	ds_read_b128 v[158:161], v2 offset:2048
	ds_read_b128 v[166:169], v2 offset:3072
	v_add_u32_e32 v2, s19, v162
	ds_read_b128 v[170:173], v2
	ds_read_b128 v[174:177], v2 offset:1024
	ds_read_b128 v[178:181], v2 offset:2048
	ds_read_b128 v[182:185], v2 offset:3072
	s_add_u32 s62, s62, 0x80000
	s_addc_u32 s63, s63, 0
	s_mov_b32 m0, s73
	v_lshl_add_u64 v[8:9], s[62:63], 0, v[134:135]
	ds_read_b128 v[186:189], v164 offset:32768
	ds_read_b128 v[190:193], v164 offset:33792
	ds_read_b128 v[194:197], v164 offset:34816
	ds_read_b128 v[198:201], v164 offset:35840
	ds_read_b128 v[202:205], v164 offset:36864
	ds_read_b128 v[206:209], v164 offset:37888
	ds_read_b128 v[210:213], v164 offset:38912
	ds_read_b128 v[214:217], v164 offset:39936
	global_load_lds_dwordx4 v[8:9], off
	v_lshl_add_u64 v[8:9], s[62:63], 0, v[138:139]
	s_mov_b32 m0, s74
	s_nop 0
	global_load_lds_dwordx4 v[8:9], off
	s_waitcnt vmcnt(8)
	s_waitcnt lgkmcnt(0)
	s_barrier
	s_setprio 1
	s_waitcnt lgkmcnt(0)
	v_mfma_f32_16x16x32_bf16 v[130:133], v[150:153], v[186:189], v[130:133]
	v_mfma_f32_16x16x32_bf16 v[126:129], v[158:161], v[186:189], v[126:129]
	v_mfma_f32_16x16x32_bf16 v[122:125], v[150:153], v[194:197], v[122:125]
	v_mfma_f32_16x16x32_bf16 v[118:121], v[158:161], v[194:197], v[118:121]
	v_mfma_f32_16x16x32_bf16 v[114:117], v[150:153], v[202:205], v[114:117]
	v_mfma_f32_16x16x32_bf16 v[110:113], v[158:161], v[202:205], v[110:113]
	v_mfma_f32_16x16x32_bf16 v[106:109], v[150:153], v[210:213], v[106:109]
	v_mfma_f32_16x16x32_bf16 v[102:105], v[158:161], v[210:213], v[102:105]
	v_mfma_f32_16x16x32_bf16 v[130:133], v[154:157], v[190:193], v[130:133]
	v_mfma_f32_16x16x32_bf16 v[126:129], v[166:169], v[190:193], v[126:129]
	v_mfma_f32_16x16x32_bf16 v[122:125], v[154:157], v[198:201], v[122:125]
	v_mfma_f32_16x16x32_bf16 v[118:121], v[166:169], v[198:201], v[118:121]
	v_mfma_f32_16x16x32_bf16 v[114:117], v[154:157], v[206:209], v[114:117]
	v_mfma_f32_16x16x32_bf16 v[110:113], v[166:169], v[206:209], v[110:113]
	v_mfma_f32_16x16x32_bf16 v[106:109], v[154:157], v[214:217], v[106:109]
	v_mfma_f32_16x16x32_bf16 v[102:105], v[166:169], v[214:217], v[102:105]
	s_setprio 0
	s_setprio 1
	v_mfma_f32_16x16x32_bf16 v[98:101], v[170:173], v[186:189], v[98:101]
	v_mfma_f32_16x16x32_bf16 v[94:97], v[178:181], v[186:189], v[94:97]
	v_mfma_f32_16x16x32_bf16 v[90:93], v[170:173], v[194:197], v[90:93]
	v_mfma_f32_16x16x32_bf16 v[86:89], v[178:181], v[194:197], v[86:89]
	v_mfma_f32_16x16x32_bf16 v[82:85], v[170:173], v[202:205], v[82:85]
	v_mfma_f32_16x16x32_bf16 v[78:81], v[178:181], v[202:205], v[78:81]
	v_mfma_f32_16x16x32_bf16 v[74:77], v[170:173], v[210:213], v[74:77]
	v_mfma_f32_16x16x32_bf16 v[70:73], v[178:181], v[210:213], v[70:73]
	v_mfma_f32_16x16x32_bf16 v[98:101], v[174:177], v[190:193], v[98:101]
	v_mfma_f32_16x16x32_bf16 v[94:97], v[182:185], v[190:193], v[94:97]
	v_mfma_f32_16x16x32_bf16 v[90:93], v[174:177], v[198:201], v[90:93]
	v_mfma_f32_16x16x32_bf16 v[86:89], v[182:185], v[198:201], v[86:89]
	v_mfma_f32_16x16x32_bf16 v[82:85], v[174:177], v[206:209], v[82:85]
	v_mfma_f32_16x16x32_bf16 v[78:81], v[182:185], v[206:209], v[78:81]
	v_mfma_f32_16x16x32_bf16 v[74:77], v[174:177], v[214:217], v[74:77]
	v_mfma_f32_16x16x32_bf16 v[70:73], v[182:185], v[214:217], v[70:73]
	s_setprio 0
	s_add_i32 s18, s18, s70
	v_lshl_add_u64 v[8:9], v[218:219], 0, s[14:15]
	s_mov_b32 m0, s18
	s_barrier
	ds_read_b128 v[186:189], v164 offset:49152
	ds_read_b128 v[190:193], v164 offset:50176
	ds_read_b128 v[194:197], v164 offset:51200
	ds_read_b128 v[198:201], v164 offset:52224
	ds_read_b128 v[202:205], v164 offset:53248
	ds_read_b128 v[206:209], v164 offset:54272
	ds_read_b128 v[210:213], v164 offset:55296
	ds_read_b128 v[214:217], v164 offset:56320
	global_load_lds_dwordx4 v[8:9], off
	s_add_i32 m0, s18, 0x2000
	s_add_u32 s58, s58, 0x80080
	v_lshl_add_u64 v[8:9], v[220:221], 0, s[14:15]
	s_addc_u32 s59, s59, 0
	s_add_i32 s18, s19, s70
	global_load_lds_dwordx4 v[8:9], off
	v_lshl_add_u64 v[8:9], s[58:59], 0, v[136:137]
	s_mov_b32 m0, s18
	s_nop 0
	global_load_lds_dwordx4 v[8:9], off
	v_lshl_add_u64 v[8:9], s[58:59], 0, v[140:141]
	s_add_i32 m0, s18, 0x2000
	s_nop 0
	global_load_lds_dwordx4 v[8:9], off
	v_lshl_add_u64 v[8:9], v[222:223], 0, s[14:15]
	s_mov_b32 m0, s75
	s_nop 0
	global_load_lds_dwordx4 v[8:9], off
	v_lshl_add_u64 v[8:9], v[224:225], 0, s[14:15]
	s_mov_b32 m0, s76
	s_nop 0
	global_load_lds_dwordx4 v[8:9], off
	s_waitcnt vmcnt(8)
	s_waitcnt lgkmcnt(0)
	s_barrier
	s_setprio 1
	s_waitcnt lgkmcnt(0)
	v_mfma_f32_16x16x32_bf16 v[66:69], v[150:153], v[186:189], v[66:69]
	v_mfma_f32_16x16x32_bf16 v[62:65], v[158:161], v[186:189], v[62:65]
	v_mfma_f32_16x16x32_bf16 v[58:61], v[150:153], v[194:197], v[58:61]
	v_mfma_f32_16x16x32_bf16 v[54:57], v[158:161], v[194:197], v[54:57]
	v_mfma_f32_16x16x32_bf16 v[50:53], v[150:153], v[202:205], v[50:53]
	v_mfma_f32_16x16x32_bf16 v[46:49], v[158:161], v[202:205], v[46:49]
	v_mfma_f32_16x16x32_bf16 v[42:45], v[150:153], v[210:213], v[42:45]
	v_mfma_f32_16x16x32_bf16 v[38:41], v[158:161], v[210:213], v[38:41]
	v_mfma_f32_16x16x32_bf16 v[66:69], v[154:157], v[190:193], v[66:69]
	v_mfma_f32_16x16x32_bf16 v[62:65], v[166:169], v[190:193], v[62:65]
	v_mfma_f32_16x16x32_bf16 v[58:61], v[154:157], v[198:201], v[58:61]
	v_mfma_f32_16x16x32_bf16 v[54:57], v[166:169], v[198:201], v[54:57]
	v_mfma_f32_16x16x32_bf16 v[50:53], v[154:157], v[206:209], v[50:53]
	v_mfma_f32_16x16x32_bf16 v[46:49], v[166:169], v[206:209], v[46:49]
	v_mfma_f32_16x16x32_bf16 v[42:45], v[154:157], v[214:217], v[42:45]
	v_mfma_f32_16x16x32_bf16 v[38:41], v[166:169], v[214:217], v[38:41]
	s_setprio 0
	s_setprio 1
	v_mfma_f32_16x16x32_bf16 v[34:37], v[170:173], v[186:189], v[34:37]
	v_mfma_f32_16x16x32_bf16 v[30:33], v[178:181], v[186:189], v[30:33]
	v_mfma_f32_16x16x32_bf16 v[26:29], v[170:173], v[194:197], v[26:29]
	v_mfma_f32_16x16x32_bf16 v[22:25], v[178:181], v[194:197], v[22:25]
	v_mfma_f32_16x16x32_bf16 v[18:21], v[170:173], v[202:205], v[18:21]
	v_mfma_f32_16x16x32_bf16 v[14:17], v[178:181], v[202:205], v[14:17]
	v_mfma_f32_16x16x32_bf16 v[8:11], v[170:173], v[210:213], v[10:13]
	v_mfma_f32_16x16x32_bf16 v[4:7], v[178:181], v[210:213], v[4:7]
	v_mfma_f32_16x16x32_bf16 v[34:37], v[174:177], v[190:193], v[34:37]
	v_mfma_f32_16x16x32_bf16 v[30:33], v[182:185], v[190:193], v[30:33]
	v_mfma_f32_16x16x32_bf16 v[26:29], v[174:177], v[198:201], v[26:29]
	v_mfma_f32_16x16x32_bf16 v[22:25], v[182:185], v[198:201], v[22:25]
	v_mfma_f32_16x16x32_bf16 v[18:21], v[174:177], v[206:209], v[18:21]
	v_mfma_f32_16x16x32_bf16 v[14:17], v[182:185], v[206:209], v[14:17]
	v_mfma_f32_16x16x32_bf16 v[10:13], v[174:177], v[214:217], v[8:11]
	v_mfma_f32_16x16x32_bf16 v[6:9], v[182:185], v[214:217], v[4:7]
	s_setprio 0
	s_add_i32 s87, s87, 2
	s_add_u32 s54, s54, 0x100
	s_addc_u32 s55, s55, 0
	s_add_u32 s57, s57, 0x100
	s_addc_u32 s86, s86, 0
	s_cmp_gt_u32 s87, 29
	s_barrier
	s_cbranch_scc0 .LBB0_846
	s_and_b64 vcc, exec, s[16:17]
	s_cbranch_vccz .LBB0_849
	s_barrier

.LBB0_927:
	ds_read_b128 v[130:133], v166
	ds_read_b128 v[134:137], v166 offset:1024
	ds_read_b128 v[138:141], v166 offset:2048
	ds_read_b128 v[142:145], v166 offset:3072
	ds_read_b128 v[170:173], v167
	ds_read_b128 v[174:177], v167 offset:1024
	ds_read_b128 v[178:181], v167 offset:2048
	ds_read_b128 v[182:185], v167 offset:3072
	s_add_u32 s18, s56, 0xfff80080
	s_addc_u32 s19, s57, -1
	s_cmp_eq_u32 s86, 28
	s_cselect_b32 s63, s47, s19
	s_cselect_b32 s62, s82, s18
	s_cselect_b32 s59, s45, s85
	s_cselect_b32 s58, s83, s84
	v_lshl_add_u64 v[162:163], s[56:57], 0, v[154:155]
	s_add_i32 m0, s55, 0xc000
	ds_read_b128 v[186:189], v168
	ds_read_b128 v[190:193], v168 offset:1024
	ds_read_b128 v[194:197], v168 offset:2048
	ds_read_b128 v[198:201], v168 offset:3072
	ds_read_b128 v[202:205], v168 offset:4096
	ds_read_b128 v[206:209], v168 offset:5120
	ds_read_b128 v[210:213], v168 offset:6144
	ds_read_b128 v[214:217], v168 offset:7168
	global_load_lds_dwordx4 v[162:163], off
	v_lshl_add_u64 v[162:163], s[56:57], 0, v[156:157]
	s_add_i32 m0, s55, 0xe000
	s_nop 0
	global_load_lds_dwordx4 v[162:163], off
	s_waitcnt vmcnt(8)
	s_waitcnt lgkmcnt(0)
	s_barrier
	s_setprio 1
	s_waitcnt lgkmcnt(0)
	v_mfma_f32_16x16x32_bf16 v[122:125], v[130:133], v[186:189], v[122:125]
	v_mfma_f32_16x16x32_bf16 v[126:129], v[138:141], v[186:189], v[126:129]
	v_mfma_f32_16x16x32_bf16 v[114:117], v[130:133], v[194:197], v[114:117]
	v_mfma_f32_16x16x32_bf16 v[118:121], v[138:141], v[194:197], v[118:121]
	v_mfma_f32_16x16x32_bf16 v[102:105], v[130:133], v[202:205], v[102:105]
	v_mfma_f32_16x16x32_bf16 v[110:113], v[138:141], v[202:205], v[110:113]
	v_mfma_f32_16x16x32_bf16 v[94:97], v[130:133], v[210:213], v[94:97]
	v_mfma_f32_16x16x32_bf16 v[74:77], v[138:141], v[210:213], v[74:77]
	v_mfma_f32_16x16x32_bf16 v[122:125], v[134:137], v[190:193], v[122:125]
	v_mfma_f32_16x16x32_bf16 v[126:129], v[142:145], v[190:193], v[126:129]
	v_mfma_f32_16x16x32_bf16 v[114:117], v[134:137], v[198:201], v[114:117]
	v_mfma_f32_16x16x32_bf16 v[118:121], v[142:145], v[198:201], v[118:121]
	v_mfma_f32_16x16x32_bf16 v[102:105], v[134:137], v[206:209], v[102:105]
	v_mfma_f32_16x16x32_bf16 v[110:113], v[142:145], v[206:209], v[110:113]
	v_mfma_f32_16x16x32_bf16 v[94:97], v[134:137], v[214:217], v[94:97]
	v_mfma_f32_16x16x32_bf16 v[74:77], v[142:145], v[214:217], v[74:77]
	s_setprio 0
	s_setprio 1
	v_mfma_f32_16x16x32_bf16 v[106:109], v[170:173], v[186:189], v[106:109]
	v_mfma_f32_16x16x32_bf16 v[90:93], v[178:181], v[186:189], v[90:93]
	v_mfma_f32_16x16x32_bf16 v[98:101], v[170:173], v[194:197], v[98:101]
	v_mfma_f32_16x16x32_bf16 v[82:85], v[178:181], v[194:197], v[82:85]
	v_mfma_f32_16x16x32_bf16 v[86:89], v[170:173], v[202:205], v[86:89]
	v_mfma_f32_16x16x32_bf16 v[78:81], v[178:181], v[202:205], v[78:81]
	v_mfma_f32_16x16x32_bf16 v[70:73], v[170:173], v[210:213], v[70:73]
	v_mfma_f32_16x16x32_bf16 v[66:69], v[178:181], v[210:213], v[66:69]
	v_mfma_f32_16x16x32_bf16 v[106:109], v[174:177], v[190:193], v[106:109]
	v_mfma_f32_16x16x32_bf16 v[90:93], v[182:185], v[190:193], v[90:93]
	v_mfma_f32_16x16x32_bf16 v[98:101], v[174:177], v[198:201], v[98:101]
	v_mfma_f32_16x16x32_bf16 v[82:85], v[182:185], v[198:201], v[82:85]
	v_mfma_f32_16x16x32_bf16 v[86:89], v[174:177], v[206:209], v[86:89]
	v_mfma_f32_16x16x32_bf16 v[78:81], v[182:185], v[206:209], v[78:81]
	v_mfma_f32_16x16x32_bf16 v[70:73], v[174:177], v[214:217], v[70:73]
	v_mfma_f32_16x16x32_bf16 v[66:69], v[182:185], v[214:217], v[66:69]
	s_setprio 0
	s_add_i32 s18, s74, s66
	v_lshl_add_u64 v[162:163], s[58:59], 0, v[148:149]
	s_mov_b32 m0, s18
	s_barrier
	ds_read_b128 v[186:189], v168 offset:16384
	ds_read_b128 v[190:193], v168 offset:17408
	ds_read_b128 v[194:197], v168 offset:18432
	ds_read_b128 v[198:201], v168 offset:19456
	ds_read_b128 v[202:205], v168 offset:20480
	ds_read_b128 v[206:209], v168 offset:21504
	ds_read_b128 v[210:213], v168 offset:22528
	ds_read_b128 v[214:217], v168 offset:23552
	global_load_lds_dwordx4 v[162:163], off
	s_add_i32 m0, s18, 0x2000
	s_add_u32 s90, s58, 0x80000
	v_lshl_add_u64 v[218:219], s[58:59], 0, v[152:153]
	s_addc_u32 s91, s59, 0
	s_add_i32 s18, s75, s66
	global_load_lds_dwordx4 v[218:219], off
	v_lshl_add_u64 v[220:221], s[90:91], 0, v[148:149]
	s_mov_b32 m0, s18
	v_lshl_add_u64 v[222:223], s[62:63], 0, v[150:151]
	global_load_lds_dwordx4 v[220:221], off
	v_lshl_add_u64 v[220:221], s[90:91], 0, v[152:153]
	s_add_i32 m0, s18, 0x2000
	s_nop 0
	global_load_lds_dwordx4 v[220:221], off
	v_lshl_add_u64 v[220:221], s[62:63], 0, v[146:147]
	s_mov_b32 m0, s55
	s_nop 0
	global_load_lds_dwordx4 v[220:221], off
	s_mov_b32 m0, s67
	s_nop 0
	global_load_lds_dwordx4 v[222:223], off
	s_waitcnt vmcnt(8)
	s_waitcnt lgkmcnt(0)
	s_barrier
	s_setprio 1
	s_waitcnt lgkmcnt(0)
	v_mfma_f32_16x16x32_bf16 v[62:65], v[130:133], v[186:189], v[62:65]
	v_mfma_f32_16x16x32_bf16 v[58:61], v[138:141], v[186:189], v[58:61]
	v_mfma_f32_16x16x32_bf16 v[50:53], v[130:133], v[194:197], v[50:53]
	v_mfma_f32_16x16x32_bf16 v[42:45], v[138:141], v[194:197], v[42:45]
	v_mfma_f32_16x16x32_bf16 v[34:37], v[130:133], v[202:205], v[34:37]
	v_mfma_f32_16x16x32_bf16 v[26:29], v[138:141], v[202:205], v[26:29]
	v_mfma_f32_16x16x32_bf16 v[18:21], v[130:133], v[210:213], v[18:21]
	v_mfma_f32_16x16x32_bf16 v[10:13], v[138:141], v[210:213], v[10:13]
	v_mfma_f32_16x16x32_bf16 v[62:65], v[134:137], v[190:193], v[62:65]
	v_mfma_f32_16x16x32_bf16 v[58:61], v[142:145], v[190:193], v[58:61]
	v_mfma_f32_16x16x32_bf16 v[50:53], v[134:137], v[198:201], v[50:53]
	v_mfma_f32_16x16x32_bf16 v[42:45], v[142:145], v[198:201], v[42:45]
	v_mfma_f32_16x16x32_bf16 v[34:37], v[134:137], v[206:209], v[34:37]
	v_mfma_f32_16x16x32_bf16 v[26:29], v[142:145], v[206:209], v[26:29]
	v_mfma_f32_16x16x32_bf16 v[18:21], v[134:137], v[214:217], v[18:21]
	v_mfma_f32_16x16x32_bf16 v[10:13], v[142:145], v[214:217], v[10:13]
	s_setprio 0
	s_setprio 1
	v_mfma_f32_16x16x32_bf16 v[54:57], v[170:173], v[186:189], v[54:57]
	v_mfma_f32_16x16x32_bf16 v[46:49], v[178:181], v[186:189], v[46:49]
	v_mfma_f32_16x16x32_bf16 v[38:41], v[170:173], v[194:197], v[38:41]
	v_mfma_f32_16x16x32_bf16 v[30:33], v[178:181], v[194:197], v[30:33]
	v_mfma_f32_16x16x32_bf16 v[22:25], v[170:173], v[202:205], v[22:25]
	v_mfma_f32_16x16x32_bf16 v[14:17], v[178:181], v[202:205], v[14:17]
	v_mfma_f32_16x16x32_bf16 v[6:9], v[170:173], v[210:213], v[6:9]
	v_mfma_f32_16x16x32_bf16 v[2:5], v[178:181], v[210:213], v[2:5]
	v_mfma_f32_16x16x32_bf16 v[54:57], v[174:177], v[190:193], v[54:57]
	v_mfma_f32_16x16x32_bf16 v[46:49], v[182:185], v[190:193], v[46:49]
	v_mfma_f32_16x16x32_bf16 v[38:41], v[174:177], v[198:201], v[38:41]
	v_mfma_f32_16x16x32_bf16 v[30:33], v[182:185], v[198:201], v[30:33]
	v_mfma_f32_16x16x32_bf16 v[22:25], v[174:177], v[206:209], v[22:25]
	v_mfma_f32_16x16x32_bf16 v[14:17], v[182:185], v[206:209], v[14:17]
	v_mfma_f32_16x16x32_bf16 v[6:9], v[174:177], v[214:217], v[6:9]
	v_mfma_f32_16x16x32_bf16 v[2:5], v[182:185], v[214:217], v[2:5]
	s_setprio 0
	s_add_i32 s18, 0, 0x18000
	s_add_i32 s19, 0, 0x1c000
	s_barrier
	v_add_u32_e32 v142, s18, v164
	v_add_u32_e32 v169, s19, v164
	ds_read_b128 v[130:133], v142
	ds_read_b128 v[134:137], v142 offset:1024
	ds_read_b128 v[138:141], v142 offset:2048
	ds_read_b128 v[142:145], v142 offset:3072
	ds_read_b128 v[170:173], v169
	ds_read_b128 v[174:177], v169 offset:1024
	ds_read_b128 v[178:181], v169 offset:2048
	ds_read_b128 v[182:185], v169 offset:3072
	s_add_u32 s62, s62, 0x80000
	s_addc_u32 s63, s63, 0
	s_mov_b32 m0, s68
	v_lshl_add_u64 v[224:225], s[62:63], 0, v[146:147]
	ds_read_b128 v[186:189], v168 offset:32768
	ds_read_b128 v[190:193], v168 offset:33792
	ds_read_b128 v[194:197], v168 offset:34816
	ds_read_b128 v[198:201], v168 offset:35840
	ds_read_b128 v[202:205], v168 offset:36864
	ds_read_b128 v[206:209], v168 offset:37888
	ds_read_b128 v[210:213], v168 offset:38912
	ds_read_b128 v[214:217], v168 offset:39936
	global_load_lds_dwordx4 v[224:225], off
	v_lshl_add_u64 v[224:225], s[62:63], 0, v[150:151]
	s_mov_b32 m0, s69
	s_nop 0
	global_load_lds_dwordx4 v[224:225], off
	s_waitcnt vmcnt(8)
	s_waitcnt lgkmcnt(0)
	s_barrier
	s_setprio 1
	s_waitcnt lgkmcnt(0)
	v_mfma_f32_16x16x32_bf16 v[122:125], v[130:133], v[186:189], v[122:125]
	v_mfma_f32_16x16x32_bf16 v[126:129], v[138:141], v[186:189], v[126:129]
	v_mfma_f32_16x16x32_bf16 v[114:117], v[130:133], v[194:197], v[114:117]
	v_mfma_f32_16x16x32_bf16 v[118:121], v[138:141], v[194:197], v[118:121]
	v_mfma_f32_16x16x32_bf16 v[102:105], v[130:133], v[202:205], v[102:105]
	v_mfma_f32_16x16x32_bf16 v[110:113], v[138:141], v[202:205], v[110:113]
	v_mfma_f32_16x16x32_bf16 v[94:97], v[130:133], v[210:213], v[94:97]
	v_mfma_f32_16x16x32_bf16 v[74:77], v[138:141], v[210:213], v[74:77]
	v_mfma_f32_16x16x32_bf16 v[122:125], v[134:137], v[190:193], v[122:125]
	v_mfma_f32_16x16x32_bf16 v[126:129], v[142:145], v[190:193], v[126:129]
	v_mfma_f32_16x16x32_bf16 v[114:117], v[134:137], v[198:201], v[114:117]
	v_mfma_f32_16x16x32_bf16 v[118:121], v[142:145], v[198:201], v[118:121]
	v_mfma_f32_16x16x32_bf16 v[102:105], v[134:137], v[206:209], v[102:105]
	v_mfma_f32_16x16x32_bf16 v[110:113], v[142:145], v[206:209], v[110:113]
	v_mfma_f32_16x16x32_bf16 v[94:97], v[134:137], v[214:217], v[94:97]
	v_mfma_f32_16x16x32_bf16 v[74:77], v[142:145], v[214:217], v[74:77]
	s_setprio 0
	s_setprio 1
	v_mfma_f32_16x16x32_bf16 v[106:109], v[170:173], v[186:189], v[106:109]
	v_mfma_f32_16x16x32_bf16 v[90:93], v[178:181], v[186:189], v[90:93]
	v_mfma_f32_16x16x32_bf16 v[98:101], v[170:173], v[194:197], v[98:101]
	v_mfma_f32_16x16x32_bf16 v[82:85], v[178:181], v[194:197], v[82:85]
	v_mfma_f32_16x16x32_bf16 v[86:89], v[170:173], v[202:205], v[86:89]
	v_mfma_f32_16x16x32_bf16 v[78:81], v[178:181], v[202:205], v[78:81]
	v_mfma_f32_16x16x32_bf16 v[70:73], v[170:173], v[210:213], v[70:73]
	v_mfma_f32_16x16x32_bf16 v[66:69], v[178:181], v[210:213], v[66:69]
	v_mfma_f32_16x16x32_bf16 v[106:109], v[174:177], v[190:193], v[106:109]
	v_mfma_f32_16x16x32_bf16 v[90:93], v[182:185], v[190:193], v[90:93]
	v_mfma_f32_16x16x32_bf16 v[98:101], v[174:177], v[198:201], v[98:101]
	v_mfma_f32_16x16x32_bf16 v[82:85], v[182:185], v[198:201], v[82:85]
	v_mfma_f32_16x16x32_bf16 v[86:89], v[174:177], v[206:209], v[86:89]
	v_mfma_f32_16x16x32_bf16 v[78:81], v[182:185], v[206:209], v[78:81]
	v_mfma_f32_16x16x32_bf16 v[70:73], v[174:177], v[214:217], v[70:73]
	v_mfma_f32_16x16x32_bf16 v[66:69], v[182:185], v[214:217], v[66:69]
	s_setprio 0
	s_add_i32 s18, s18, s66
	v_lshl_add_u64 v[162:163], v[162:163], 0, s[12:13]
	s_mov_b32 m0, s18
	s_barrier
	ds_read_b128 v[186:189], v168 offset:49152
	ds_read_b128 v[190:193], v168 offset:50176
	ds_read_b128 v[194:197], v168 offset:51200
	ds_read_b128 v[198:201], v168 offset:52224
	ds_read_b128 v[202:205], v168 offset:53248
	ds_read_b128 v[206:209], v168 offset:54272
	ds_read_b128 v[210:213], v168 offset:55296
	ds_read_b128 v[214:217], v168 offset:56320
	global_load_lds_dwordx4 v[162:163], off
	s_add_i32 m0, s18, 0x2000
	s_add_u32 s58, s58, 0x80080
	v_lshl_add_u64 v[162:163], v[218:219], 0, s[12:13]
	s_addc_u32 s59, s59, 0
	s_add_i32 s18, s19, s66
	global_load_lds_dwordx4 v[162:163], off
	v_lshl_add_u64 v[162:163], s[58:59], 0, v[148:149]
	s_mov_b32 m0, s18
	s_nop 0
	global_load_lds_dwordx4 v[162:163], off
	v_lshl_add_u64 v[162:163], s[58:59], 0, v[152:153]
	s_add_i32 m0, s18, 0x2000
	s_nop 0
	global_load_lds_dwordx4 v[162:163], off
	v_lshl_add_u64 v[162:163], v[220:221], 0, s[12:13]
	s_mov_b32 m0, s72
	s_nop 0
	global_load_lds_dwordx4 v[162:163], off
	v_lshl_add_u64 v[162:163], v[222:223], 0, s[12:13]
	s_mov_b32 m0, s73
	s_nop 0
	global_load_lds_dwordx4 v[162:163], off
	s_waitcnt vmcnt(8)
	s_waitcnt lgkmcnt(0)
	s_barrier
	s_setprio 1
	s_waitcnt lgkmcnt(0)
	v_mfma_f32_16x16x32_bf16 v[62:65], v[130:133], v[186:189], v[62:65]
	v_mfma_f32_16x16x32_bf16 v[58:61], v[138:141], v[186:189], v[58:61]
	v_mfma_f32_16x16x32_bf16 v[50:53], v[130:133], v[194:197], v[50:53]
	v_mfma_f32_16x16x32_bf16 v[42:45], v[138:141], v[194:197], v[42:45]
	v_mfma_f32_16x16x32_bf16 v[34:37], v[130:133], v[202:205], v[34:37]
	v_mfma_f32_16x16x32_bf16 v[26:29], v[138:141], v[202:205], v[26:29]
	v_mfma_f32_16x16x32_bf16 v[18:21], v[130:133], v[210:213], v[18:21]
	v_mfma_f32_16x16x32_bf16 v[10:13], v[138:141], v[210:213], v[10:13]
	v_mfma_f32_16x16x32_bf16 v[62:65], v[134:137], v[190:193], v[62:65]
	v_mfma_f32_16x16x32_bf16 v[58:61], v[142:145], v[190:193], v[58:61]
	v_mfma_f32_16x16x32_bf16 v[50:53], v[134:137], v[198:201], v[50:53]
	v_mfma_f32_16x16x32_bf16 v[42:45], v[142:145], v[198:201], v[42:45]
	v_mfma_f32_16x16x32_bf16 v[34:37], v[134:137], v[206:209], v[34:37]
	v_mfma_f32_16x16x32_bf16 v[26:29], v[142:145], v[206:209], v[26:29]
	v_mfma_f32_16x16x32_bf16 v[18:21], v[134:137], v[214:217], v[18:21]
	v_mfma_f32_16x16x32_bf16 v[10:13], v[142:145], v[214:217], v[10:13]
	s_setprio 0
	s_setprio 1
	v_mfma_f32_16x16x32_bf16 v[54:57], v[170:173], v[186:189], v[54:57]
	v_mfma_f32_16x16x32_bf16 v[46:49], v[178:181], v[186:189], v[46:49]
	v_mfma_f32_16x16x32_bf16 v[38:41], v[170:173], v[194:197], v[38:41]
	v_mfma_f32_16x16x32_bf16 v[30:33], v[178:181], v[194:197], v[30:33]
	v_mfma_f32_16x16x32_bf16 v[22:25], v[170:173], v[202:205], v[22:25]
	v_mfma_f32_16x16x32_bf16 v[14:17], v[178:181], v[202:205], v[14:17]
	v_mfma_f32_16x16x32_bf16 v[6:9], v[170:173], v[210:213], v[6:9]
	v_mfma_f32_16x16x32_bf16 v[2:5], v[178:181], v[210:213], v[2:5]
	v_mfma_f32_16x16x32_bf16 v[54:57], v[174:177], v[190:193], v[54:57]
	v_mfma_f32_16x16x32_bf16 v[46:49], v[182:185], v[190:193], v[46:49]
	v_mfma_f32_16x16x32_bf16 v[38:41], v[174:177], v[198:201], v[38:41]
	v_mfma_f32_16x16x32_bf16 v[30:33], v[182:185], v[198:201], v[30:33]
	v_mfma_f32_16x16x32_bf16 v[22:25], v[174:177], v[206:209], v[22:25]
	v_mfma_f32_16x16x32_bf16 v[14:17], v[182:185], v[206:209], v[14:17]
	v_mfma_f32_16x16x32_bf16 v[6:9], v[174:177], v[214:217], v[6:9]
	v_mfma_f32_16x16x32_bf16 v[2:5], v[182:185], v[214:217], v[2:5]
	s_setprio 0
	s_add_i32 s86, s86, 2
	s_add_u32 s56, s56, 0x100
	s_addc_u32 s57, s57, 0
	s_add_u32 s84, s84, 0x100
	s_addc_u32 s85, s85, 0
	s_cmp_gt_u32 s86, 29
	s_barrier
	s_cbranch_scc0 .LBB0_927
	s_and_b64 vcc, exec, s[14:15]
	s_cbranch_vccz .LBB0_930
	s_barrier

.LBB0_1172:
	v_add_u32_e32 v14, 0x14000, v221
	ds_read_b128 v[18:21], v222
	ds_read_b128 v[22:25], v222 offset:1024
	ds_read_b128 v[26:29], v222 offset:2048
	ds_read_b128 v[30:33], v222 offset:3072
	ds_read_b128 v[2:5], v14
	ds_read_b128 v[6:9], v14 offset:1024
	ds_read_b128 v[10:13], v14 offset:2048
	ds_read_b128 v[14:17], v14 offset:3072
	v_lshl_add_u64 v[68:69], s[58:59], 0, v[208:209]
	s_add_i32 m0, s70, 0xc000
	s_waitcnt lgkmcnt(0)
	ds_read_b128 v[34:37], v223
	ds_read_b128 v[38:41], v223 offset:1024
	ds_read_b128 v[42:45], v223 offset:2048
	ds_read_b128 v[46:49], v223 offset:3072
	ds_read_b128 v[50:53], v223 offset:4096
	ds_read_b128 v[54:57], v223 offset:5120
	ds_read_b128 v[58:61], v223 offset:6144
	ds_read_b128 v[62:65], v223 offset:7168
	global_load_lds_dwordx4 v[68:69], off
	v_lshl_add_u64 v[68:69], s[58:59], 0, v[210:211]
	s_add_i32 m0, s70, 0xe000
	s_nop 0
	global_load_lds_dwordx4 v[68:69], off
	s_waitcnt vmcnt(8)
	s_waitcnt lgkmcnt(0)
	s_barrier
	s_setprio 1
	s_waitcnt lgkmcnt(0)
	v_mfma_scale_f32_16x16x128_f8f6f4 v[194:197], v[18:25], v[34:41], v[194:197], v220, v220 op_sel_hi:[0,0,0]
	v_mfma_scale_f32_16x16x128_f8f6f4 v[186:189], v[26:33], v[34:41], v[186:189], v220, v220 op_sel_hi:[0,0,0]
	v_mfma_scale_f32_16x16x128_f8f6f4 v[178:181], v[18:25], v[42:49], v[178:181], v220, v220 op_sel_hi:[0,0,0]
	v_mfma_scale_f32_16x16x128_f8f6f4 v[170:173], v[26:33], v[42:49], v[170:173], v220, v220 op_sel_hi:[0,0,0]
	v_mfma_scale_f32_16x16x128_f8f6f4 v[162:165], v[18:25], v[50:57], v[162:165], v220, v220 op_sel_hi:[0,0,0]
	v_mfma_scale_f32_16x16x128_f8f6f4 v[154:157], v[26:33], v[50:57], v[154:157], v220, v220 op_sel_hi:[0,0,0]
	v_mfma_scale_f32_16x16x128_f8f6f4 v[146:149], v[18:25], v[58:65], v[146:149], v220, v220 op_sel_hi:[0,0,0]
	v_mfma_scale_f32_16x16x128_f8f6f4 v[138:141], v[26:33], v[58:65], v[138:141], v220, v220 op_sel_hi:[0,0,0]
	s_setprio 0
	s_setprio 1
	v_mfma_scale_f32_16x16x128_f8f6f4 v[190:193], v[2:9], v[34:41], v[190:193], v220, v220 op_sel_hi:[0,0,0]
	v_mfma_scale_f32_16x16x128_f8f6f4 v[182:185], v[10:17], v[34:41], v[182:185], v220, v220 op_sel_hi:[0,0,0]
	v_mfma_scale_f32_16x16x128_f8f6f4 v[174:177], v[2:9], v[42:49], v[174:177], v220, v220 op_sel_hi:[0,0,0]
	v_mfma_scale_f32_16x16x128_f8f6f4 v[166:169], v[10:17], v[42:49], v[166:169], v220, v220 op_sel_hi:[0,0,0]
	v_mfma_scale_f32_16x16x128_f8f6f4 v[158:161], v[2:9], v[50:57], v[158:161], v220, v220 op_sel_hi:[0,0,0]
	v_mfma_scale_f32_16x16x128_f8f6f4 v[150:153], v[10:17], v[50:57], v[150:153], v220, v220 op_sel_hi:[0,0,0]
	v_mfma_scale_f32_16x16x128_f8f6f4 v[142:145], v[2:9], v[58:65], v[142:145], v220, v220 op_sel_hi:[0,0,0]
	v_mfma_scale_f32_16x16x128_f8f6f4 v[134:137], v[10:17], v[58:65], v[134:137], v220, v220 op_sel_hi:[0,0,0]
	s_setprio 0
	v_cndmask_b32_e64 v67, 0, 1, s[8:9]
	v_cmp_ne_u32_e64 s[6:7], 1, v67
	s_andn2_b64 vcc, exec, s[8:9]
	s_barrier
	s_cbranch_vccnz .LBB0_1174
	ds_read_b128 v[34:37], v223 offset:16384
	ds_read_b128 v[38:41], v223 offset:17408
	ds_read_b128 v[42:45], v223 offset:18432
	ds_read_b128 v[46:49], v223 offset:19456
	ds_read_b128 v[50:53], v223 offset:20480
	ds_read_b128 v[54:57], v223 offset:21504
	ds_read_b128 v[58:61], v223 offset:22528
	ds_read_b128 v[62:65], v223 offset:23552

.LBB0_1176:
	s_barrier
	v_add_u32_e32 v2, 0x18000, v221
	v_add_u32_e32 v14, 0x1c000, v221
	ds_read_b128 v[18:21], v2
	ds_read_b128 v[22:25], v2 offset:1024
	ds_read_b128 v[26:29], v2 offset:2048
	ds_read_b128 v[30:33], v2 offset:3072
	ds_read_b128 v[2:5], v14
	ds_read_b128 v[6:9], v14 offset:1024
	ds_read_b128 v[10:13], v14 offset:2048
	ds_read_b128 v[14:17], v14 offset:3072
	s_add_u32 s62, s62, 0x40000
	s_addc_u32 s63, s63, 0
	s_mov_b32 m0, s76
	v_lshl_add_u64 v[226:227], s[62:63], 0, v[200:201]
	s_waitcnt lgkmcnt(0)
	ds_read_b128 v[34:37], v223 offset:32768
	ds_read_b128 v[38:41], v223 offset:33792
	ds_read_b128 v[42:45], v223 offset:34816
	ds_read_b128 v[46:49], v223 offset:35840
	ds_read_b128 v[50:53], v223 offset:36864
	ds_read_b128 v[54:57], v223 offset:37888
	ds_read_b128 v[58:61], v223 offset:38912
	ds_read_b128 v[62:65], v223 offset:39936
	global_load_lds_dwordx4 v[226:227], off
	v_lshl_add_u64 v[226:227], s[62:63], 0, v[202:203]
	s_mov_b32 m0, s77
	s_nop 0
	global_load_lds_dwordx4 v[226:227], off
	s_waitcnt vmcnt(8)
	s_waitcnt lgkmcnt(0)
	s_barrier
	s_setprio 1
	s_waitcnt lgkmcnt(0)
	v_mfma_scale_f32_16x16x128_f8f6f4 v[194:197], v[18:25], v[34:41], v[194:197], v220, v220 op_sel_hi:[0,0,0]
	v_mfma_scale_f32_16x16x128_f8f6f4 v[186:189], v[26:33], v[34:41], v[186:189], v220, v220 op_sel_hi:[0,0,0]
	v_mfma_scale_f32_16x16x128_f8f6f4 v[178:181], v[18:25], v[42:49], v[178:181], v220, v220 op_sel_hi:[0,0,0]
	v_mfma_scale_f32_16x16x128_f8f6f4 v[170:173], v[26:33], v[42:49], v[170:173], v220, v220 op_sel_hi:[0,0,0]
	v_mfma_scale_f32_16x16x128_f8f6f4 v[162:165], v[18:25], v[50:57], v[162:165], v220, v220 op_sel_hi:[0,0,0]
	v_mfma_scale_f32_16x16x128_f8f6f4 v[154:157], v[26:33], v[50:57], v[154:157], v220, v220 op_sel_hi:[0,0,0]
	v_mfma_scale_f32_16x16x128_f8f6f4 v[146:149], v[18:25], v[58:65], v[146:149], v220, v220 op_sel_hi:[0,0,0]
	v_mfma_scale_f32_16x16x128_f8f6f4 v[138:141], v[26:33], v[58:65], v[138:141], v220, v220 op_sel_hi:[0,0,0]
	s_setprio 0
	s_setprio 1
	v_mfma_scale_f32_16x16x128_f8f6f4 v[190:193], v[2:9], v[34:41], v[190:193], v220, v220 op_sel_hi:[0,0,0]
	v_mfma_scale_f32_16x16x128_f8f6f4 v[182:185], v[10:17], v[34:41], v[182:185], v220, v220 op_sel_hi:[0,0,0]
	v_mfma_scale_f32_16x16x128_f8f6f4 v[174:177], v[2:9], v[42:49], v[174:177], v220, v220 op_sel_hi:[0,0,0]
	v_mfma_scale_f32_16x16x128_f8f6f4 v[166:169], v[10:17], v[42:49], v[166:169], v220, v220 op_sel_hi:[0,0,0]
	v_mfma_scale_f32_16x16x128_f8f6f4 v[158:161], v[2:9], v[50:57], v[158:161], v220, v220 op_sel_hi:[0,0,0]
	v_mfma_scale_f32_16x16x128_f8f6f4 v[150:153], v[10:17], v[50:57], v[150:153], v220, v220 op_sel_hi:[0,0,0]
	v_mfma_scale_f32_16x16x128_f8f6f4 v[142:145], v[2:9], v[58:65], v[142:145], v220, v220 op_sel_hi:[0,0,0]
	v_mfma_scale_f32_16x16x128_f8f6f4 v[134:137], v[10:17], v[58:65], v[134:137], v220, v220 op_sel_hi:[0,0,0]
	s_setprio 0
	s_and_b64 vcc, exec, s[6:7]
	s_barrier
	s_cbranch_vccnz .LBB0_1178
	ds_read_b128 v[34:37], v223 offset:49152
	ds_read_b128 v[38:41], v223 offset:50176
	ds_read_b128 v[42:45], v223 offset:51200
	ds_read_b128 v[46:49], v223 offset:52224
	ds_read_b128 v[50:53], v223 offset:53248
	ds_read_b128 v[54:57], v223 offset:54272
	ds_read_b128 v[58:61], v223 offset:55296
	ds_read_b128 v[62:65], v223 offset:56320

.LBB0_1296:
	v_add_u32_e32 v2, 0x10000, v232
	v_add_u32_e32 v14, 0x14000, v232
	ds_read_b128 v[18:21], v2
	ds_read_b128 v[22:25], v2 offset:1024
	ds_read_b128 v[26:29], v2 offset:2048
	ds_read_b128 v[30:33], v2 offset:3072
	ds_read_b128 v[2:5], v14
	ds_read_b128 v[6:9], v14 offset:1024
	ds_read_b128 v[10:13], v14 offset:2048
	ds_read_b128 v[14:17], v14 offset:3072
	v_lshl_add_u64 v[68:69], s[64:65], 0, v[210:211]
	s_add_i32 m0, s63, 0xc000
	s_waitcnt lgkmcnt(0)
	ds_read_b128 v[34:37], v233
	ds_read_b128 v[38:41], v233 offset:1024
	ds_read_b128 v[42:45], v233 offset:2048
	ds_read_b128 v[46:49], v233 offset:3072
	ds_read_b128 v[50:53], v233 offset:4096
	ds_read_b128 v[54:57], v233 offset:5120
	ds_read_b128 v[58:61], v233 offset:6144
	ds_read_b128 v[62:65], v233 offset:7168
	global_load_lds_dwordx4 v[68:69], off
	v_lshl_add_u64 v[68:69], s[64:65], 0, v[212:213]
	s_add_i32 m0, s63, 0xe000
	s_nop 0
	global_load_lds_dwordx4 v[68:69], off
	s_waitcnt vmcnt(8)
	s_waitcnt lgkmcnt(0)
	s_barrier
	s_setprio 1
	s_waitcnt lgkmcnt(0)
	v_mfma_scale_f32_16x16x128_f8f6f4 v[194:197], v[18:25], v[34:41], v[194:197], v231, v231 op_sel_hi:[0,0,0]
	v_mfma_scale_f32_16x16x128_f8f6f4 v[190:193], v[26:33], v[34:41], v[190:193], v231, v231 op_sel_hi:[0,0,0]
	v_mfma_scale_f32_16x16x128_f8f6f4 v[186:189], v[18:25], v[42:49], v[186:189], v231, v231 op_sel_hi:[0,0,0]
	v_mfma_scale_f32_16x16x128_f8f6f4 v[182:185], v[26:33], v[42:49], v[182:185], v231, v231 op_sel_hi:[0,0,0]
	v_mfma_scale_f32_16x16x128_f8f6f4 v[166:169], v[18:25], v[50:57], v[166:169], v231, v231 op_sel_hi:[0,0,0]
	v_mfma_scale_f32_16x16x128_f8f6f4 v[158:161], v[26:33], v[50:57], v[158:161], v231, v231 op_sel_hi:[0,0,0]
	v_mfma_scale_f32_16x16x128_f8f6f4 v[154:157], v[18:25], v[58:65], v[154:157], v231, v231 op_sel_hi:[0,0,0]
	v_mfma_scale_f32_16x16x128_f8f6f4 v[150:153], v[26:33], v[58:65], v[150:153], v231, v231 op_sel_hi:[0,0,0]
	s_setprio 0
	s_setprio 1
	v_mfma_scale_f32_16x16x128_f8f6f4 v[178:181], v[2:9], v[34:41], v[178:181], v231, v231 op_sel_hi:[0,0,0]
	v_mfma_scale_f32_16x16x128_f8f6f4 v[174:177], v[10:17], v[34:41], v[174:177], v231, v231 op_sel_hi:[0,0,0]
	v_mfma_scale_f32_16x16x128_f8f6f4 v[170:173], v[2:9], v[42:49], v[170:173], v231, v231 op_sel_hi:[0,0,0]
	v_mfma_scale_f32_16x16x128_f8f6f4 v[162:165], v[10:17], v[42:49], v[162:165], v231, v231 op_sel_hi:[0,0,0]
	v_mfma_scale_f32_16x16x128_f8f6f4 v[146:149], v[2:9], v[50:57], v[146:149], v231, v231 op_sel_hi:[0,0,0]
	v_mfma_scale_f32_16x16x128_f8f6f4 v[142:145], v[10:17], v[50:57], v[142:145], v231, v231 op_sel_hi:[0,0,0]
	v_mfma_scale_f32_16x16x128_f8f6f4 v[138:141], v[2:9], v[58:65], v[138:141], v231, v231 op_sel_hi:[0,0,0]
	v_mfma_scale_f32_16x16x128_f8f6f4 v[134:137], v[10:17], v[58:65], v[134:137], v231, v231 op_sel_hi:[0,0,0]
	s_setprio 0
	v_cndmask_b32_e64 v66, 0, 1, s[8:9]
	v_cmp_ne_u32_e64 s[10:11], 1, v66
	s_andn2_b64 vcc, exec, s[8:9]
	s_barrier
	s_cbranch_vccnz .LBB0_1298
	ds_read_b128 v[34:37], v233 offset:16384
	ds_read_b128 v[38:41], v233 offset:17408
	ds_read_b128 v[42:45], v233 offset:18432
	ds_read_b128 v[46:49], v233 offset:19456
	ds_read_b128 v[50:53], v233 offset:20480
	ds_read_b128 v[54:57], v233 offset:21504
	ds_read_b128 v[58:61], v233 offset:22528
	ds_read_b128 v[62:65], v233 offset:23552

.LBB0_1300:
	s_barrier
	v_add_u32_e32 v2, 0x18000, v232
	v_add_u32_e32 v14, 0x1c000, v232
	ds_read_b128 v[18:21], v2
	ds_read_b128 v[22:25], v2 offset:1024
	ds_read_b128 v[26:29], v2 offset:2048
	ds_read_b128 v[30:33], v2 offset:3072
	ds_read_b128 v[2:5], v14
	ds_read_b128 v[6:9], v14 offset:1024
	ds_read_b128 v[10:13], v14 offset:2048
	ds_read_b128 v[14:17], v14 offset:3072
	s_add_u32 s66, s66, 0x40000
	s_addc_u32 s67, s67, 0
	s_mov_b32 m0, s75
	v_lshl_add_u64 v[238:239], s[66:67], 0, v[202:203]
	s_waitcnt lgkmcnt(0)
	ds_read_b128 v[34:37], v233 offset:32768
	ds_read_b128 v[38:41], v233 offset:33792
	ds_read_b128 v[42:45], v233 offset:34816
	ds_read_b128 v[46:49], v233 offset:35840
	ds_read_b128 v[50:53], v233 offset:36864
	ds_read_b128 v[54:57], v233 offset:37888
	ds_read_b128 v[58:61], v233 offset:38912
	ds_read_b128 v[62:65], v233 offset:39936
	global_load_lds_dwordx4 v[238:239], off
	v_lshl_add_u64 v[238:239], s[66:67], 0, v[204:205]
	s_mov_b32 m0, s76
	s_nop 0
	global_load_lds_dwordx4 v[238:239], off
	s_waitcnt vmcnt(8)
	s_waitcnt lgkmcnt(0)
	s_barrier
	s_setprio 1
	s_waitcnt lgkmcnt(0)
	v_mfma_scale_f32_16x16x128_f8f6f4 v[194:197], v[18:25], v[34:41], v[194:197], v231, v231 op_sel_hi:[0,0,0]
	v_mfma_scale_f32_16x16x128_f8f6f4 v[190:193], v[26:33], v[34:41], v[190:193], v231, v231 op_sel_hi:[0,0,0]
	v_mfma_scale_f32_16x16x128_f8f6f4 v[186:189], v[18:25], v[42:49], v[186:189], v231, v231 op_sel_hi:[0,0,0]
	v_mfma_scale_f32_16x16x128_f8f6f4 v[182:185], v[26:33], v[42:49], v[182:185], v231, v231 op_sel_hi:[0,0,0]
	v_mfma_scale_f32_16x16x128_f8f6f4 v[166:169], v[18:25], v[50:57], v[166:169], v231, v231 op_sel_hi:[0,0,0]
	v_mfma_scale_f32_16x16x128_f8f6f4 v[158:161], v[26:33], v[50:57], v[158:161], v231, v231 op_sel_hi:[0,0,0]
	v_mfma_scale_f32_16x16x128_f8f6f4 v[154:157], v[18:25], v[58:65], v[154:157], v231, v231 op_sel_hi:[0,0,0]
	v_mfma_scale_f32_16x16x128_f8f6f4 v[150:153], v[26:33], v[58:65], v[150:153], v231, v231 op_sel_hi:[0,0,0]
	s_setprio 0
	s_setprio 1
	v_mfma_scale_f32_16x16x128_f8f6f4 v[178:181], v[2:9], v[34:41], v[178:181], v231, v231 op_sel_hi:[0,0,0]
	v_mfma_scale_f32_16x16x128_f8f6f4 v[174:177], v[10:17], v[34:41], v[174:177], v231, v231 op_sel_hi:[0,0,0]
	v_mfma_scale_f32_16x16x128_f8f6f4 v[170:173], v[2:9], v[42:49], v[170:173], v231, v231 op_sel_hi:[0,0,0]
	v_mfma_scale_f32_16x16x128_f8f6f4 v[162:165], v[10:17], v[42:49], v[162:165], v231, v231 op_sel_hi:[0,0,0]
	v_mfma_scale_f32_16x16x128_f8f6f4 v[146:149], v[2:9], v[50:57], v[146:149], v231, v231 op_sel_hi:[0,0,0]
	v_mfma_scale_f32_16x16x128_f8f6f4 v[142:145], v[10:17], v[50:57], v[142:145], v231, v231 op_sel_hi:[0,0,0]
	v_mfma_scale_f32_16x16x128_f8f6f4 v[138:141], v[2:9], v[58:65], v[138:141], v231, v231 op_sel_hi:[0,0,0]
	v_mfma_scale_f32_16x16x128_f8f6f4 v[134:137], v[10:17], v[58:65], v[134:137], v231, v231 op_sel_hi:[0,0,0]
	s_setprio 0
	s_and_b64 vcc, exec, s[10:11]
	s_barrier
	s_cbranch_vccnz .LBB0_1302
	ds_read_b128 v[34:37], v233 offset:49152
	ds_read_b128 v[38:41], v233 offset:50176
	ds_read_b128 v[42:45], v233 offset:51200
	ds_read_b128 v[46:49], v233 offset:52224
	ds_read_b128 v[50:53], v233 offset:53248
	ds_read_b128 v[54:57], v233 offset:54272
	ds_read_b128 v[58:61], v233 offset:55296
	ds_read_b128 v[62:65], v233 offset:56320
